# P13 diff-attn tile loop: K fragment reads issued up front with counted lgkmcnt waits, first V group prefetched before softmax, PV groups keep next group reads in flight
# speedup vs baseline: 1.0049x; 1.0049x over previous
; __device__ __forceinline__ void bt_load(const float* __restrict__ src, int N, int perm, int it, int ntn, f32x4 (&v)[8]) {
;     const int wid = threadIdx.x >> 6, lane = threadIdx.x & 63;
;     const int per = 16 * ntn, z = it / per, r = it % per, kt = r / ntn, nt = r % ntn;
;     const int np = nt * 256 + lane * 4;
;     const int sc = perm ? (nt * 128 + (lane & 31) * 4 + (lane >> 5) * 1024) : np;
;     const float* p = src + (size_t)z * 1024 * N + (size_t)(kt * 64 + wid * 8) * N + sc;
; #pragma unroll
;     for (int i = 0; i < 8; ++i) v[i] = __builtin_nontemporal_load((const f32x4*)(p + (size_t)i * N));
; }
; __device__ __forceinline__ void ph_big_transpose(const float* __restrict__ src, int N, int perm, int batch, bf16* __restrict__ dst, float* tile  , int G, int ndefer) {
;     const int tid = threadIdx.x, wid = tid >> 6, lane = tid & 63, ntn = N / 256, total = batch * 16 * ntn - ndefer;
;     int it = (int)blockIdx.x;
;     if (it >= total) return;
;     f32x4 cur[8], nxt[8], nx2[8];
;     bt_load(src, N, perm, it, ntn, cur);
;     if (it + G < total) bt_load(src, N, perm, it + G, ntn, nxt);
.LBB0_63:
	s_cmpk_gt_i32 s2, 0x1a87
	s_waitcnt lgkmcnt(0)
	s_barrier
	s_cbranch_scc1 .LBB0_71
	s_ashr_i32 s0, s2, 31
	s_lshr_b32 s0, s0, 25
	s_add_i32 s1, s2, s0
	s_ashr_i32 s0, s1, 7
	s_and_b32 s1, s1, 0xff80
	s_sub_i32 s1, s2, s1
	s_bfe_i32 s4, s1, 0x80000
	s_bfe_u32 s4, s4, 0x3000c
	s_add_i32 s4, s1, s4
	s_bfe_i32 s5, s4, 0x80000
	s_and_b32 s4, s4, 0xf8
	v_lshlrev_b32_e32 v2, 2, v0
	s_sub_i32 s1, s1, s4
	v_and_b32_e32 v2, 0x7c, v2
	v_lshlrev_b32_e32 v3, 5, v0
	s_movk_i32 s4, 0x400
	s_sext_i32_i8 s1, s1
	v_and_or_b32 v99, v3, s4, v2
	v_lshl_add_u32 v2, s1, 7, v99
	s_ashr_i32 s1, s0, 31
	s_lshl_b64 s[0:1], s[0:1], 23
	s_sext_i32_i16 s5, s5
	s_add_u32 s0, s68, s0
	s_addc_u32 s1, s69, s1
	s_lshl_b32 s4, s5, 3
	v_lshrrev_b32_e32 v3, 3, v0
	s_andn2_b32 s4, s4, 63
	v_and_b32_e32 v110, 56, v3
	v_or_b32_e32 v4, s4, v110
	v_ashrrev_i32_e32 v5, 31, v4
	v_lshlrev_b64 v[4:5], 13, v[4:5]
	v_lshl_add_u64 v[4:5], s[0:1], 0, v[4:5]
	v_ashrrev_i32_e32 v3, 31, v2
	v_lshl_add_u64 v[2:3], v[2:3], 2, v[4:5]
	s_movk_i32 s0, 0x2000
	v_add_co_u32_e32 v4, vcc, s0, v2
	s_movk_i32 s1, 0x4000
	s_nop 0
	v_addc_co_u32_e32 v5, vcc, 0, v3, vcc
	global_load_dwordx4 v[38:41], v[2:3], off nt
	global_load_dwordx4 v[34:37], v[4:5], off nt
	v_add_co_u32_e32 v4, vcc, s1, v2
	s_movk_i32 s4, 0x6000
	s_nop 0
	v_addc_co_u32_e32 v5, vcc, 0, v3, vcc
	v_add_co_u32_e32 v6, vcc, s4, v2
	s_mov_b32 s5, 0x8000
	s_nop 0
	v_addc_co_u32_e32 v7, vcc, 0, v3, vcc
	global_load_dwordx4 v[46:49], v[4:5], off nt
	global_load_dwordx4 v[42:45], v[6:7], off nt
	v_add_co_u32_e32 v4, vcc, s5, v2
	s_mov_b32 s6, 0xa000
	s_nop 0
	v_addc_co_u32_e32 v5, vcc, 0, v3, vcc
	v_add_co_u32_e32 v6, vcc, s6, v2
	s_add_i32 s6, s62, s2
	s_nop 0
	v_addc_co_u32_e32 v7, vcc, 0, v3, vcc
	global_load_dwordx4 v[54:57], v[4:5], off nt
	global_load_dwordx4 v[50:53], v[6:7], off nt
	v_add_co_u32_e32 v4, vcc, 0xc000, v2
	s_cmpk_gt_i32 s6, 0x1a87
	s_nop 0
	v_addc_co_u32_e32 v5, vcc, 0, v3, vcc
	v_add_co_u32_e32 v2, vcc, 0xe000, v2
	s_nop 1
	v_addc_co_u32_e32 v3, vcc, 0, v3, vcc
	global_load_dwordx4 v[62:65], v[4:5], off nt
	global_load_dwordx4 v[58:61], v[2:3], off nt
	s_cbranch_scc1 .LBB0_66
	s_ashr_i32 s7, s6, 31
	s_lshr_b32 s7, s7, 25
	s_add_i32 s7, s6, s7
	s_ashr_i32 s8, s7, 7
	s_and_b32 s7, s7, 0xff80
	s_sub_i32 s6, s6, s7
	s_bfe_i32 s7, s6, 0x80000
	s_bfe_u32 s7, s7, 0x3000c
	s_add_i32 s7, s6, s7
	s_bfe_i32 s9, s7, 0x80000
	s_and_b32 s7, s7, 0xf8
	s_sub_i32 s6, s6, s7
	s_sext_i32_i16 s10, s9
	s_sext_i32_i8 s6, s6
	s_ashr_i32 s9, s8, 31
	v_lshl_add_u32 v2, s6, 7, v99
	s_lshl_b64 s[6:7], s[8:9], 23
	s_add_u32 s6, s68, s6
	s_addc_u32 s7, s69, s7
	s_lshl_b32 s8, s10, 3
	s_andn2_b32 s8, s8, 63
	v_or_b32_e32 v4, s8, v110
	v_ashrrev_i32_e32 v5, 31, v4
	v_lshlrev_b64 v[4:5], 13, v[4:5]
	v_lshl_add_u64 v[4:5], s[6:7], 0, v[4:5]
	v_ashrrev_i32_e32 v3, 31, v2
	v_lshl_add_u64 v[26:27], v[2:3], 2, v[4:5]
	v_add_co_u32_e32 v6, vcc, s0, v26
	s_nop 1
	v_addc_co_u32_e32 v7, vcc, 0, v27, vcc
	v_add_co_u32_e32 v10, vcc, s1, v26
	global_load_dwordx4 v[2:5], v[26:27], off nt
	s_nop 0
	global_load_dwordx4 v[6:9], v[6:7], off nt
	v_addc_co_u32_e32 v11, vcc, 0, v27, vcc
	v_add_co_u32_e32 v14, vcc, s4, v26
	s_nop 1
	v_addc_co_u32_e32 v15, vcc, 0, v27, vcc
	v_add_co_u32_e32 v18, vcc, s5, v26
	global_load_dwordx4 v[10:13], v[10:11], off nt
	s_nop 0
	global_load_dwordx4 v[14:17], v[14:15], off nt
	v_addc_co_u32_e32 v19, vcc, 0, v27, vcc
	v_add_co_u32_e32 v22, vcc, 0xa000, v26
	s_nop 1
	v_addc_co_u32_e32 v23, vcc, 0, v27, vcc
	v_add_co_u32_e32 v28, vcc, 0xc000, v26
	global_load_dwordx4 v[18:21], v[18:19], off nt
	s_nop 0
	global_load_dwordx4 v[22:25], v[22:23], off nt
	v_addc_co_u32_e32 v29, vcc, 0, v27, vcc
	v_add_co_u32_e32 v30, vcc, 0xe000, v26
	s_nop 1
	v_addc_co_u32_e32 v31, vcc, 0, v27, vcc
	global_load_dwordx4 v[26:29], v[28:29], off nt
	s_nop 0
	global_load_dwordx4 v[30:33], v[30:31], off nt

; __device__ __forceinline__ unsigned g8_cvt_pk(float lo, float hi) { unsigned r; asm volatile("v_cvt_pk_bf16_f32 %0, %1, %2" : "=v"(r) : "v"(lo), "v"(hi)); return r; }
; __device__ __forceinline__ void ph_big_transpose(const float* __restrict__ src, int N, int perm, int batch, bf16* __restrict__ dst, float* tile  , int G, int ndefer) {
;     ...
;     for (; it < total; it += G) {
;         const bool more = it + G < total, more2 = it + 2 * G < total;
;         if (more2) bt_load(src, N, perm, it + 2 * G, ntn, nx2);
;         __syncthreads();
; #pragma unroll
;         for (int i = 0; i < 8; ++i) { float* t = tile + (wid * 8 + i) * 257 + lane * 4; t[0] = cur[i][0]; t[1] = cur[i][1]; t[2] = cur[i][2]; t[3] = cur[i][3]; }
;         __syncthreads();
;         const int per = 16 * ntn, z = it / per, r = it % per, kt = r / ntn, nt = r % ntn;
;         bf16* d = dst + (size_t)z * N * 1024 + (((size_t)nt * 16 + kt) << 14);
;         const int kc = lane & 7;
; #pragma unroll
;         for (int pss = 0; pss < 4; ++pss) {
;             const int n = wid * 32 + pss * 8 + (lane >> 3); float f[8];
; #pragma unroll
;             for (int j = 0; j < 8; ++j) f[j] = tile[(kc * 8 + j) * 257 + n];
;             u32x4 w; w.x = g8_cvt_pk(f[0], f[1]); w.y = g8_cvt_pk(f[2], f[3]); w.z = g8_cvt_pk(f[4], f[5]); w.w = g8_cvt_pk(f[6], f[7]);
;             __builtin_nontemporal_store(w, (u32x4*)(d + n * 64 + kc * 8));
;         }
;         if (more) {
; #pragma unroll
;             for (int i = 0; i < 8; ++i) { cur[i] = nxt[i]; nxt[i] = nx2[i]; } }
;     }
.LBB0_67:
	s_barrier
	s_waitcnt vmcnt(7)
	ds_write_b128 v111, v[38:41]
	v_add_u32_e32 v38, 0x404, v111
	s_ashr_i32 s9, s8, 31
	s_waitcnt vmcnt(6)
	ds_write2_b32 v38, v34, v35 offset1:1
	v_add_u32_e32 v34, 0x40c, v111
	s_lshr_b32 s9, s9, 25
	ds_write2_b32 v34, v36, v37 offset1:1
	v_add_u32_e32 v34, 0x808, v111
	s_add_i32 s9, s8, s9
	s_waitcnt vmcnt(5)
	ds_write2_b64 v34, v[46:47], v[48:49] offset1:1
	v_add_u32_e32 v34, 0xc0c, v111
	s_ashr_i32 s10, s9, 7
	s_and_b32 s9, s9, 0xff80
	s_waitcnt vmcnt(4)
	ds_write2_b32 v34, v42, v43 offset1:1
	v_add_u32_e32 v34, 0xc14, v111
	s_sub_i32 s9, s8, s9
	s_add_i32 s31, s8, s62
	ds_write2_b32 v34, v44, v45 offset1:1
	s_waitcnt vmcnt(3)
	ds_write_b128 v111, v[54:57] offset:4112
	v_add_u32_e32 v34, 0x1414, v111
	s_bfe_i32 s8, s9, 0x80000
	s_waitcnt vmcnt(2)
	ds_write2_b32 v34, v50, v51 offset1:1
	v_add_u32_e32 v34, 0x141c, v111
	s_bfe_u32 s8, s8, 0x3000c
	ds_write2_b32 v34, v52, v53 offset1:1
	v_add_u32_e32 v34, 0x1818, v111
	s_add_i32 s11, s9, s8
	s_waitcnt vmcnt(1)
	ds_write2_b64 v34, v[62:63], v[64:65] offset1:1
	v_add_u32_e32 v34, 0x1c1c, v111
	s_bfe_i32 s8, s11, 0x80000
	s_and_b32 s11, s11, 0xf8
	s_waitcnt vmcnt(0)
	ds_write2_b32 v34, v58, v59 offset1:1
	v_add_u32_e32 v34, 0x1c24, v111
	s_sext_i32_i16 s8, s8
	s_sub_i32 s30, s9, s11
	s_ashr_i32 s11, s10, 31
	ds_write2_b32 v34, v60, v61 offset1:1
	s_waitcnt lgkmcnt(0)
	s_barrier
	s_lshr_b32 s8, s8, 3
	s_lshl_b64 s[10:11], s[10:11], 22
	ds_read_b32 v34, v112 offset:1028
	ds_read_b32 v35, v112 offset:3084
	ds_read_b32 v36, v112 offset:5140
	ds_read_b32 v37, v112 offset:7196
	ds_read_b32 v38, v112 offset:6168
	ds_read_b32 v39, v112 offset:4112
	ds_read_b32 v40, v112 offset:2056
	ds_read_b32 v41, v112
	s_add_u32 s33, s5, s10
	s_addc_u32 s34, s6, s11
	s_bfe_i64 s[10:11], s[30:31], 0x80000
	s_bfe_i64 s[8:9], s[8:9], 0x100000
	s_lshl_b64 s[10:11], s[10:11], 19
	s_add_u32 s10, s33, s10
	s_addc_u32 s11, s34, s11
	s_lshl_b64 s[8:9], s[8:9], 15
	s_waitcnt lgkmcnt(0)
	v_cvt_pk_bf16_f32 v34, v41, v34
	v_cvt_pk_bf16_f32 v35, v40, v35
	v_cvt_pk_bf16_f32 v36, v39, v36
	v_cvt_pk_bf16_f32 v37, v38, v37
	ds_read_b32 v42, v112 offset:1060
	ds_read_b32 v43, v112 offset:3116
	ds_read_b32 v44, v112 offset:5172
	ds_read_b32 v45, v112 offset:7228
	ds_read_b32 v46, v112 offset:6200
	ds_read_b32 v47, v112 offset:4144
	ds_read_b32 v48, v112 offset:2088
	ds_read_b32 v49, v112 offset:32
	s_add_u32 s8, s10, s8
	s_addc_u32 s9, s11, s9
	v_lshl_add_u64 v[38:39], s[8:9], 0, v[100:101]
	v_mov_b32_e32 v103, v101
	v_lshl_add_u64 v[40:41], v[38:39], 0, v[102:103]
	global_store_dwordx4 v[40:41], v[34:37], off nt
	v_mov_b32_e32 v105, v101
	v_lshl_add_u64 v[40:41], v[38:39], 0, v[104:105]
	s_waitcnt lgkmcnt(0)
	v_cvt_pk_bf16_f32 v34, v49, v42
	v_cvt_pk_bf16_f32 v35, v48, v43
	v_cvt_pk_bf16_f32 v36, v47, v44
	v_cvt_pk_bf16_f32 v37, v46, v45
	ds_read_b32 v42, v112 offset:1092
	ds_read_b32 v43, v112 offset:3148
	ds_read_b32 v44, v112 offset:5204
	ds_read_b32 v45, v112 offset:6232
	ds_read_b32 v46, v112 offset:4176
	ds_read_b32 v47, v112 offset:2120
	ds_read_b32 v48, v112 offset:64
	ds_read_b32 v49, v112 offset:7260
	global_store_dwordx4 v[40:41], v[34:37], off nt
	v_mov_b32_e32 v107, v101
	v_lshl_add_u64 v[40:41], v[38:39], 0, v[106:107]
	s_waitcnt lgkmcnt(1)
	v_cvt_pk_bf16_f32 v34, v48, v42
	v_cvt_pk_bf16_f32 v35, v47, v43
	v_cvt_pk_bf16_f32 v36, v46, v44
	s_waitcnt lgkmcnt(0)
	v_cvt_pk_bf16_f32 v37, v45, v49
	ds_read_b32 v42, v112 offset:1124
	ds_read_b32 v43, v112 offset:3180
	ds_read_b32 v44, v112 offset:5236
	ds_read_b32 v45, v112 offset:6264
	ds_read_b32 v46, v112 offset:4208
	ds_read_b32 v47, v112 offset:2152
	ds_read_b32 v48, v112 offset:96
	ds_read_b32 v49, v112 offset:7292
	v_mov_b32_e32 v109, v101
	global_store_dwordx4 v[40:41], v[34:37], off nt
	v_lshl_add_u64 v[38:39], v[38:39], 0, v[108:109]
	v_mov_b64_e32 v[60:61], v[32:33]
	s_waitcnt lgkmcnt(1)
	v_cvt_pk_bf16_f32 v34, v48, v42
	v_cvt_pk_bf16_f32 v35, v47, v43
	v_cvt_pk_bf16_f32 v36, v46, v44
	s_waitcnt lgkmcnt(0)
	v_cvt_pk_bf16_f32 v37, v45, v49
	global_store_dwordx4 v[38:39], v[34:37], off nt
	v_mov_b64_e32 v[64:65], v[28:29]
	v_mov_b64_e32 v[52:53], v[24:25]
	v_mov_b64_e32 v[56:57], v[20:21]
	v_mov_b64_e32 v[44:45], v[16:17]
	v_mov_b64_e32 v[48:49], v[12:13]
	v_mov_b64_e32 v[36:37], v[8:9]
	v_mov_b64_e32 v[40:41], v[4:5]
	v_mov_b64_e32 v[58:59], v[30:31]
	v_mov_b64_e32 v[62:63], v[26:27]
	v_mov_b64_e32 v[50:51], v[22:23]
	v_mov_b64_e32 v[54:55], v[18:19]
	v_mov_b64_e32 v[42:43], v[14:15]
	v_mov_b64_e32 v[46:47], v[10:11]
	v_mov_b64_e32 v[34:35], v[6:7]
	v_mov_b64_e32 v[38:39], v[2:3]
	v_mov_b64_e32 v[30:31], v[94:95]
	v_mov_b64_e32 v[26:27], v[90:91]
	v_mov_b64_e32 v[22:23], v[86:87]
	v_mov_b64_e32 v[18:19], v[82:83]
	v_mov_b64_e32 v[14:15], v[78:79]
	v_mov_b64_e32 v[10:11], v[74:75]
	v_mov_b64_e32 v[6:7], v[70:71]
	v_mov_b64_e32 v[2:3], v[66:67]
	s_cmpk_lt_i32 s31, 0x1a88
	v_mov_b64_e32 v[32:33], v[96:97]
	v_mov_b64_e32 v[28:29], v[92:93]
	v_mov_b64_e32 v[24:25], v[88:89]
	v_mov_b64_e32 v[20:21], v[84:85]
	v_mov_b64_e32 v[16:17], v[80:81]
	v_mov_b64_e32 v[12:13], v[76:77]
	v_mov_b64_e32 v[8:9], v[72:73]
	v_mov_b64_e32 v[4:5], v[68:69]
	s_mov_b32 s8, s31
	s_cbranch_scc0 .LBB0_70
; __device__ __forceinline__ void bt_load(const float* __restrict__ src, int N, int perm, int it, int ntn, f32x4 (&v)[8]) {
;     const int wid = threadIdx.x >> 6, lane = threadIdx.x & 63;
;     const int per = 16 * ntn, z = it / per, r = it % per, kt = r / ntn, nt = r % ntn;
;     const int np = nt * 256 + lane * 4;
;     const int sc = perm ? (nt * 128 + (lane & 31) * 4 + (lane >> 5) * 1024) : np;
;     const float* p = src + (size_t)z * 1024 * N + (size_t)(kt * 64 + wid * 8) * N + sc;
; #pragma unroll
;     for (int i = 0; i < 8; ++i) v[i] = __builtin_nontemporal_load((const f32x4*)(p + (size_t)i * N));
; }
; __device__ __forceinline__ void ph_big_transpose(const float* __restrict__ src, int N, int perm, int batch, bf16* __restrict__ dst, float* tile  , int G, int ndefer) {
;     ...
;         const bool more = it + G < total, more2 = it + 2 * G < total;
;         if (more2) bt_load(src, N, perm, it + 2 * G, ntn, nx2);
.LBB0_68:
	s_add_i32 s9, s7, s8
	s_cmpk_gt_i32 s9, 0x1a87
	s_cbranch_scc1 .LBB0_67
	s_ashr_i32 s10, s9, 31
	s_lshr_b32 s10, s10, 25
	s_add_i32 s11, s9, s10
	s_ashr_i32 s10, s11, 7
	s_and_b32 s11, s11, 0xff80
	s_sub_i32 s9, s9, s11
	s_bfe_i32 s11, s9, 0x80000
	s_bfe_u32 s11, s11, 0x3000c
	s_add_i32 s11, s9, s11
	s_bfe_i32 s30, s11, 0x80000
	s_and_b32 s11, s11, 0xf8
	s_sub_i32 s9, s9, s11
	s_ashr_i32 s11, s10, 31
	s_lshl_b64 s[10:11], s[10:11], 23
	s_sext_i32_i16 s30, s30
	s_sext_i32_i8 s9, s9
	s_add_u32 s10, s68, s10
	v_lshl_add_u32 v66, s9, 7, v99
	s_addc_u32 s11, s69, s11
	s_lshl_b32 s9, s30, 3
	s_andn2_b32 s9, s9, 63
	v_or_b32_e32 v68, s9, v110
	v_ashrrev_i32_e32 v69, 31, v68
	v_lshlrev_b64 v[68:69], 13, v[68:69]
	v_lshl_add_u64 v[68:69], s[10:11], 0, v[68:69]
	v_ashrrev_i32_e32 v67, 31, v66
	v_lshl_add_u64 v[90:91], v[66:67], 2, v[68:69]
	v_add_co_u32_e32 v70, vcc, s0, v90
	s_nop 1
	v_addc_co_u32_e32 v71, vcc, 0, v91, vcc
	v_add_co_u32_e32 v74, vcc, s1, v90
	global_load_dwordx4 v[66:69], v[90:91], off nt
	s_nop 0
	global_load_dwordx4 v[70:73], v[70:71], off nt
	v_addc_co_u32_e32 v75, vcc, 0, v91, vcc
	v_add_co_u32_e32 v78, vcc, s4, v90
	s_nop 1
	v_addc_co_u32_e32 v79, vcc, 0, v91, vcc
	v_add_co_u32_e32 v82, vcc, 0x8000, v90
	global_load_dwordx4 v[74:77], v[74:75], off nt
	s_nop 0
	global_load_dwordx4 v[78:81], v[78:79], off nt
	v_addc_co_u32_e32 v83, vcc, 0, v91, vcc
	v_add_co_u32_e32 v86, vcc, 0xa000, v90
	s_nop 1
	v_addc_co_u32_e32 v87, vcc, 0, v91, vcc
	v_add_co_u32_e32 v92, vcc, 0xc000, v90
	global_load_dwordx4 v[82:85], v[82:83], off nt
	s_nop 0
	global_load_dwordx4 v[86:89], v[86:87], off nt
	v_addc_co_u32_e32 v93, vcc, 0, v91, vcc
	v_add_co_u32_e32 v94, vcc, 0xe000, v90
	s_nop 1
	v_addc_co_u32_e32 v95, vcc, 0, v91, vcc
	global_load_dwordx4 v[90:93], v[92:93], off nt
	s_nop 0
	global_load_dwordx4 v[94:97], v[94:95], off nt
	s_branch .LBB0_67

; __device__ __forceinline__ void bt_load(const float* __restrict__ src, int N, int perm, int it, int ntn, f32x4 (&v)[8]) {
;     const int wid = threadIdx.x >> 6, lane = threadIdx.x & 63;
;     const int per = 16 * ntn, z = it / per, r = it % per, kt = r / ntn, nt = r % ntn;
;     const int np = nt * 256 + lane * 4;
;     const int sc = perm ? (nt * 128 + (lane & 31) * 4 + (lane >> 5) * 1024) : np;
;     const float* p = src + (size_t)z * 1024 * N + (size_t)(kt * 64 + wid * 8) * N + sc;
; #pragma unroll
;     for (int i = 0; i < 8; ++i) v[i] = __builtin_nontemporal_load((const f32x4*)(p + (size_t)i * N));
; }
; __device__ __forceinline__ void ph_big_transpose(const float* __restrict__ src, int N, int perm, int batch, bf16* __restrict__ dst, float* tile  , int G, int ndefer) {
;     const int tid = threadIdx.x, wid = tid >> 6, lane = tid & 63, ntn = N / 256, total = batch * 16 * ntn - ndefer;
;     int it = (int)blockIdx.x;
;     if (it >= total) return;
;     f32x4 cur[8], nxt[8], nx2[8];
;     bt_load(src, N, perm, it, ntn, cur);
;     if (it + G < total) bt_load(src, N, perm, it + G, ntn, nxt);
.LBB0_71:
	s_cmpk_gt_i32 s2, 0xd43
	s_cbranch_scc1 .LBB0_79
	s_ashr_i32 s0, s2, 31
	s_lshr_b32 s0, s0, 26
	s_add_i32 s1, s2, s0
	s_ashr_i32 s0, s1, 6
	s_and_b32 s1, s1, 0xffc0
	s_sub_i32 s1, s2, s1
	s_bfe_i32 s4, s1, 0x80000
	s_bfe_u32 s4, s4, 0x2000d
	s_add_i32 s4, s1, s4
	s_bfe_i32 s5, s4, 0x80000
	s_and_b32 s4, s4, 0xfc
	s_sub_i32 s1, s1, s4
	v_lshlrev_b32_e32 v2, 2, v0
	s_sext_i32_i8 s1, s1
	v_and_b32_e32 v99, 0xfc, v2
	v_lshl_or_b32 v2, s1, 8, v99
	s_ashr_i32 s1, s0, 31
	s_lshl_b64 s[0:1], s[0:1], 22
	s_sext_i32_i16 s5, s5
	s_add_u32 s0, s72, s0
	s_addc_u32 s1, s73, s1
	s_lshl_b32 s4, s5, 4
	v_lshrrev_b32_e32 v3, 3, v0
	s_andn2_b32 s4, s4, 63
	v_and_b32_e32 v110, 56, v3
	v_or_b32_e32 v4, s4, v110
	v_ashrrev_i32_e32 v5, 31, v4
	v_lshlrev_b64 v[4:5], 12, v[4:5]
	v_lshl_add_u64 v[4:5], s[0:1], 0, v[4:5]
	v_ashrrev_i32_e32 v3, 31, v2
	v_lshl_add_u64 v[2:3], v[2:3], 2, v[4:5]
	s_movk_i32 s0, 0x2000
	v_add_co_u32_e32 v4, vcc, s0, v2
	s_movk_i32 s4, 0x4000
	s_nop 0
	v_addc_co_u32_e32 v5, vcc, 0, v3, vcc
	global_load_dwordx4 v[42:45], v[4:5], off offset:-4096 nt
	global_load_dwordx4 v[34:37], v[4:5], off nt
	v_add_co_u32_e32 v4, vcc, s4, v2
	s_movk_i32 s1, 0x5000
	s_nop 0
	v_addc_co_u32_e32 v5, vcc, 0, v3, vcc
	global_load_dwordx4 v[46:49], v[4:5], off offset:-4096 nt
	global_load_dwordx4 v[38:41], v[4:5], off nt
	v_add_co_u32_e32 v4, vcc, s1, v2
	s_add_i32 s5, s62, s2
	s_nop 0
	v_addc_co_u32_e32 v5, vcc, 0, v3, vcc
	global_load_dwordx4 v[62:65], v[2:3], off nt
	global_load_dwordx4 v[50:53], v[4:5], off nt
	v_add_co_u32_e32 v4, vcc, 0x6000, v2
	s_cmpk_gt_i32 s5, 0xd43
	s_nop 0
	v_addc_co_u32_e32 v5, vcc, 0, v3, vcc
	v_add_co_u32_e32 v2, vcc, 0x7000, v2
	s_movk_i32 s1, 0x3000
	s_nop 0
	v_addc_co_u32_e32 v3, vcc, 0, v3, vcc
	global_load_dwordx4 v[58:61], v[4:5], off nt
	global_load_dwordx4 v[54:57], v[2:3], off nt
	s_cbranch_scc1 .LBB0_74
	s_ashr_i32 s6, s5, 31
	s_lshr_b32 s6, s6, 26
	s_add_i32 s7, s5, s6
	s_ashr_i32 s6, s7, 6
	s_and_b32 s7, s7, 0xffc0
	s_sub_i32 s5, s5, s7
	s_bfe_i32 s7, s5, 0x80000
	s_bfe_u32 s7, s7, 0x2000d
	s_add_i32 s7, s5, s7
	s_bfe_i32 s8, s7, 0x80000
	s_and_b32 s7, s7, 0xfc
	s_sub_i32 s5, s5, s7
	s_ashr_i32 s7, s6, 31
	s_lshl_b64 s[6:7], s[6:7], 22
	s_sext_i32_i16 s8, s8
	s_sext_i32_i8 s5, s5
	s_add_u32 s6, s72, s6
	v_lshl_or_b32 v2, s5, 8, v99
	s_addc_u32 s7, s73, s7
	s_lshl_b32 s5, s8, 4
	s_andn2_b32 s5, s5, 63
	v_or_b32_e32 v4, s5, v110
	v_ashrrev_i32_e32 v5, 31, v4
	v_lshlrev_b64 v[4:5], 12, v[4:5]
	v_lshl_add_u64 v[4:5], s[6:7], 0, v[4:5]
	v_ashrrev_i32_e32 v3, 31, v2
	v_lshl_add_u64 v[26:27], v[2:3], 2, v[4:5]
	v_add_co_u32_e32 v2, vcc, s0, v26
	s_nop 1
	v_addc_co_u32_e32 v3, vcc, 0, v27, vcc
	v_add_co_u32_e32 v10, vcc, s4, v26
	global_load_dwordx4 v[6:9], v[2:3], off offset:-4096 nt
	s_nop 0
	global_load_dwordx4 v[2:5], v[2:3], off nt
	v_addc_co_u32_e32 v11, vcc, 0, v27, vcc
	v_add_co_u32_e32 v18, vcc, 0x5000, v26
	global_load_dwordx4 v[14:17], v[10:11], off offset:-4096 nt
	s_nop 0
	global_load_dwordx4 v[10:13], v[10:11], off nt
	v_addc_co_u32_e32 v19, vcc, 0, v27, vcc
	v_add_co_u32_e32 v28, vcc, 0x6000, v26
	global_load_dwordx4 v[22:25], v[26:27], off nt
	s_nop 0
	global_load_dwordx4 v[18:21], v[18:19], off nt
	v_addc_co_u32_e32 v29, vcc, 0, v27, vcc
	v_add_co_u32_e32 v30, vcc, 0x7000, v26
	s_nop 1
	v_addc_co_u32_e32 v31, vcc, 0, v27, vcc
	global_load_dwordx4 v[26:29], v[28:29], off nt
	s_nop 0
	global_load_dwordx4 v[30:33], v[30:31], off nt

; __device__ __forceinline__ unsigned g8_cvt_pk(float lo, float hi) { unsigned r; asm volatile("v_cvt_pk_bf16_f32 %0, %1, %2" : "=v"(r) : "v"(lo), "v"(hi)); return r; }
; __device__ __forceinline__ void ph_big_transpose(const float* __restrict__ src, int N, int perm, int batch, bf16* __restrict__ dst, float* tile  , int G, int ndefer) {
;     ...
;     for (; it < total; it += G) {
;         const bool more = it + G < total, more2 = it + 2 * G < total;
;         if (more2) bt_load(src, N, perm, it + 2 * G, ntn, nx2);
;         __syncthreads();
; #pragma unroll
;         for (int i = 0; i < 8; ++i) { float* t = tile + (wid * 8 + i) * 257 + lane * 4; t[0] = cur[i][0]; t[1] = cur[i][1]; t[2] = cur[i][2]; t[3] = cur[i][3]; }
;         __syncthreads();
;         const int per = 16 * ntn, z = it / per, r = it % per, kt = r / ntn, nt = r % ntn;
;         bf16* d = dst + (size_t)z * N * 1024 + (((size_t)nt * 16 + kt) << 14);
;         const int kc = lane & 7;
; #pragma unroll
;         for (int pss = 0; pss < 4; ++pss) {
;             const int n = wid * 32 + pss * 8 + (lane >> 3); float f[8];
; #pragma unroll
;             for (int j = 0; j < 8; ++j) f[j] = tile[(kc * 8 + j) * 257 + n];
;             u32x4 w; w.x = g8_cvt_pk(f[0], f[1]); w.y = g8_cvt_pk(f[2], f[3]); w.z = g8_cvt_pk(f[4], f[5]); w.w = g8_cvt_pk(f[6], f[7]);
;             __builtin_nontemporal_store(w, (u32x4*)(d + n * 64 + kc * 8));
;         }
;         if (more) {
; #pragma unroll
;             for (int i = 0; i < 8; ++i) { cur[i] = nxt[i]; nxt[i] = nx2[i]; } }
;     }
.LBB0_75:
	s_ashr_i32 s8, s3, 31
	s_barrier
	s_waitcnt vmcnt(3)
	ds_write_b128 v111, v[62:65]
	v_add_u32_e32 v62, 0x404, v111
	s_lshr_b32 s8, s8, 26
	ds_write2_b32 v62, v42, v43 offset1:1
	v_add_u32_e32 v42, 0x40c, v111
	s_add_i32 s9, s3, s8
	ds_write2_b32 v42, v44, v45 offset1:1
	v_add_u32_e32 v42, 0x808, v111
	s_ashr_i32 s8, s9, 6
	s_and_b32 s9, s9, 0xffc0
	s_add_i32 s7, s3, s62
	ds_write2_b64 v42, v[34:35], v[36:37] offset1:1
	v_add_u32_e32 v34, 0xc0c, v111
	s_sub_i32 s3, s3, s9
	ds_write2_b32 v34, v46, v47 offset1:1
	v_add_u32_e32 v34, 0xc14, v111
	s_bfe_i32 s9, s3, 0x80000
	ds_write2_b32 v34, v48, v49 offset1:1
	ds_write_b128 v111, v[38:41] offset:4112
	v_add_u32_e32 v34, 0x1414, v111
	s_bfe_u32 s9, s9, 0x2000d
	s_waitcnt vmcnt(2)
	ds_write2_b32 v34, v50, v51 offset1:1
	v_add_u32_e32 v34, 0x141c, v111
	s_add_i32 s9, s3, s9
	ds_write2_b32 v34, v52, v53 offset1:1
	v_add_u32_e32 v34, 0x1818, v111
	s_bfe_i32 s10, s9, 0x80000
	s_and_b32 s9, s9, 0xfc
	s_waitcnt vmcnt(1)
	ds_write2_b64 v34, v[58:59], v[60:61] offset1:1
	v_add_u32_e32 v34, 0x1c1c, v111
	s_sext_i32_i16 s10, s10
	s_sub_i32 s30, s3, s9
	s_ashr_i32 s9, s8, 31
	s_waitcnt vmcnt(0)
	ds_write2_b32 v34, v54, v55 offset1:1
	v_add_u32_e32 v34, 0x1c24, v111
	s_lshr_b32 s10, s10, 2
	s_lshl_b64 s[8:9], s[8:9], 21
	ds_write2_b32 v34, v56, v57 offset1:1
	s_waitcnt lgkmcnt(0)
	s_barrier
	s_add_u32 s3, s4, s8
	ds_read_b32 v34, v112 offset:1028
	ds_read_b32 v35, v112 offset:3084
	ds_read_b32 v36, v112 offset:5140
	ds_read_b32 v37, v112 offset:7196
	ds_read_b32 v38, v112 offset:6168
	ds_read_b32 v39, v112 offset:4112
	ds_read_b32 v40, v112 offset:2056
	ds_read_b32 v41, v112
	s_addc_u32 s31, s5, s9
	s_bfe_i64 s[8:9], s[30:31], 0x80000
	s_bfe_i64 s[10:11], s[10:11], 0x100000
	s_lshl_b64 s[8:9], s[8:9], 19
	s_add_u32 s3, s3, s8
	s_addc_u32 s30, s31, s9
	s_lshl_b64 s[8:9], s[10:11], 15
	s_waitcnt lgkmcnt(0)
	v_cvt_pk_bf16_f32 v34, v41, v34
	v_cvt_pk_bf16_f32 v35, v40, v35
	v_cvt_pk_bf16_f32 v36, v39, v36
	v_cvt_pk_bf16_f32 v37, v38, v37
	ds_read_b32 v42, v112 offset:1060
	ds_read_b32 v43, v112 offset:3116
	ds_read_b32 v44, v112 offset:5172
	ds_read_b32 v45, v112 offset:7228
	ds_read_b32 v46, v112 offset:6200
	ds_read_b32 v47, v112 offset:4144
	ds_read_b32 v48, v112 offset:2088
	ds_read_b32 v49, v112 offset:32
	s_add_u32 s8, s3, s8
	s_addc_u32 s9, s30, s9
	v_lshl_add_u64 v[38:39], s[8:9], 0, v[100:101]
	v_mov_b32_e32 v103, v101
	v_lshl_add_u64 v[40:41], v[38:39], 0, v[102:103]
	global_store_dwordx4 v[40:41], v[34:37], off nt
	v_mov_b32_e32 v105, v101
	v_lshl_add_u64 v[40:41], v[38:39], 0, v[104:105]
	s_waitcnt lgkmcnt(0)
	v_cvt_pk_bf16_f32 v34, v49, v42
	v_cvt_pk_bf16_f32 v35, v48, v43
	v_cvt_pk_bf16_f32 v36, v47, v44
	v_cvt_pk_bf16_f32 v37, v46, v45
	ds_read_b32 v42, v112 offset:1092
	ds_read_b32 v43, v112 offset:3148
	ds_read_b32 v44, v112 offset:5204
	ds_read_b32 v45, v112 offset:6232
	ds_read_b32 v46, v112 offset:4176
	ds_read_b32 v47, v112 offset:2120
	ds_read_b32 v48, v112 offset:64
	ds_read_b32 v49, v112 offset:7260
	global_store_dwordx4 v[40:41], v[34:37], off nt
	v_mov_b32_e32 v107, v101
	v_lshl_add_u64 v[40:41], v[38:39], 0, v[106:107]
	s_waitcnt lgkmcnt(1)
	v_cvt_pk_bf16_f32 v34, v48, v42
	v_cvt_pk_bf16_f32 v35, v47, v43
	v_cvt_pk_bf16_f32 v36, v46, v44
	s_waitcnt lgkmcnt(0)
	v_cvt_pk_bf16_f32 v37, v45, v49
	ds_read_b32 v42, v112 offset:1124
	ds_read_b32 v43, v112 offset:3180
	ds_read_b32 v44, v112 offset:5236
	ds_read_b32 v45, v112 offset:6264
	ds_read_b32 v46, v112 offset:4208
	ds_read_b32 v47, v112 offset:2152
	ds_read_b32 v48, v112 offset:96
	ds_read_b32 v49, v112 offset:7292
	v_mov_b32_e32 v109, v101
	global_store_dwordx4 v[40:41], v[34:37], off nt
	v_lshl_add_u64 v[38:39], v[38:39], 0, v[108:109]
	v_mov_b64_e32 v[56:57], v[32:33]
	s_waitcnt lgkmcnt(1)
	v_cvt_pk_bf16_f32 v34, v48, v42
	v_cvt_pk_bf16_f32 v35, v47, v43
	v_cvt_pk_bf16_f32 v36, v46, v44
	s_waitcnt lgkmcnt(0)
	v_cvt_pk_bf16_f32 v37, v45, v49
	global_store_dwordx4 v[38:39], v[34:37], off nt
	v_mov_b64_e32 v[60:61], v[28:29]
	v_mov_b64_e32 v[52:53], v[20:21]
	v_mov_b64_e32 v[40:41], v[12:13]
	v_mov_b64_e32 v[48:49], v[16:17]
	v_mov_b64_e32 v[36:37], v[4:5]
	v_mov_b64_e32 v[44:45], v[8:9]
	v_mov_b64_e32 v[64:65], v[24:25]
	v_mov_b64_e32 v[54:55], v[30:31]
	v_mov_b64_e32 v[58:59], v[26:27]
	v_mov_b64_e32 v[50:51], v[18:19]
	v_mov_b64_e32 v[38:39], v[10:11]
	v_mov_b64_e32 v[46:47], v[14:15]
	v_mov_b64_e32 v[34:35], v[2:3]
	v_mov_b64_e32 v[42:43], v[6:7]
	v_mov_b64_e32 v[62:63], v[22:23]
	v_mov_b64_e32 v[30:31], v[94:95]
	v_mov_b64_e32 v[26:27], v[90:91]
	v_mov_b64_e32 v[18:19], v[86:87]
	v_mov_b64_e32 v[10:11], v[82:83]
	v_mov_b64_e32 v[14:15], v[74:75]
	v_mov_b64_e32 v[2:3], v[66:67]
	v_mov_b64_e32 v[6:7], v[70:71]
	v_mov_b64_e32 v[22:23], v[78:79]
	s_cmpk_lt_i32 s7, 0xd44
	v_mov_b64_e32 v[32:33], v[96:97]
	v_mov_b64_e32 v[28:29], v[92:93]
	v_mov_b64_e32 v[20:21], v[88:89]
	v_mov_b64_e32 v[12:13], v[84:85]
	v_mov_b64_e32 v[16:17], v[76:77]
	v_mov_b64_e32 v[4:5], v[68:69]
	v_mov_b64_e32 v[8:9], v[72:73]
	v_mov_b64_e32 v[24:25], v[80:81]
	s_mov_b32 s3, s7
	s_cbranch_scc0 .LBB0_78
.LBB0_76:
	s_add_i32 s7, s6, s3
	s_cmpk_gt_i32 s7, 0xd43
	s_cbranch_scc1 .LBB0_75
	s_ashr_i32 s8, s7, 31
	s_lshr_b32 s8, s8, 26
	s_add_i32 s9, s7, s8
	s_ashr_i32 s8, s9, 6
	s_and_b32 s9, s9, 0xffc0
	s_sub_i32 s7, s7, s9
	s_bfe_i32 s9, s7, 0x80000
	s_bfe_u32 s9, s9, 0x2000d
	s_add_i32 s9, s7, s9
	s_bfe_i32 s10, s9, 0x80000
	s_and_b32 s9, s9, 0xfc
	s_sub_i32 s7, s7, s9
	s_ashr_i32 s9, s8, 31
	s_lshl_b64 s[8:9], s[8:9], 22
	s_sext_i32_i16 s10, s10
	s_sext_i32_i8 s7, s7
	s_add_u32 s8, s72, s8
	v_lshl_or_b32 v66, s7, 8, v99
	s_addc_u32 s9, s73, s9
	s_lshl_b32 s7, s10, 4
	s_andn2_b32 s7, s7, 63
	v_or_b32_e32 v68, s7, v110
	v_ashrrev_i32_e32 v69, 31, v68
	v_lshlrev_b64 v[68:69], 12, v[68:69]
	v_lshl_add_u64 v[68:69], s[8:9], 0, v[68:69]
	v_ashrrev_i32_e32 v67, 31, v66
	v_lshl_add_u64 v[90:91], v[66:67], 2, v[68:69]
	v_add_co_u32_e32 v66, vcc, s0, v90
	s_nop 1
	v_addc_co_u32_e32 v67, vcc, 0, v91, vcc
	v_add_co_u32_e32 v74, vcc, s1, v90
	global_load_dwordx4 v[70:73], v[66:67], off offset:-4096 nt
	s_nop 0
	global_load_dwordx4 v[66:69], v[66:67], off nt
	v_addc_co_u32_e32 v75, vcc, 0, v91, vcc
	v_add_co_u32_e32 v82, vcc, 0x4000, v90
	global_load_dwordx4 v[78:81], v[90:91], off nt
	s_nop 0
	global_load_dwordx4 v[74:77], v[74:75], off nt
	v_addc_co_u32_e32 v83, vcc, 0, v91, vcc
	v_add_co_u32_e32 v86, vcc, 0x5000, v90
	s_nop 1
	v_addc_co_u32_e32 v87, vcc, 0, v91, vcc
	v_add_co_u32_e32 v92, vcc, 0x6000, v90
	global_load_dwordx4 v[82:85], v[82:83], off nt
	s_nop 0
	global_load_dwordx4 v[86:89], v[86:87], off nt
	v_addc_co_u32_e32 v93, vcc, 0, v91, vcc
	v_add_co_u32_e32 v94, vcc, 0x7000, v90
	s_nop 1
	v_addc_co_u32_e32 v95, vcc, 0, v91, vcc
	global_load_dwordx4 v[90:93], v[92:93], off nt
	s_nop 0
	global_load_dwordx4 v[94:97], v[94:95], off nt
	s_branch .LBB0_75

; #define SEAM(k) do { if (IN(k) && IN((k) + 1)) xcd_barrier(bar); \
;         if (PROBE_MASK) { const unsigned long long t_ = __builtin_amdgcn_s_memrealtime(); if ((PROBE_MASK >> (k)) & 1u) pr_acc += t_ - pr_t0; pr_t0 = t_; } } while (0)
; __device__ __forceinline__ void convert_deferred(const Ptrs& P, unsigned char* lds, int quota) {
;     const int tid = threadIdx.x, wid = tid >> 6, lane = tid & 63;
;     float* tile = (float*)lds;
;     volatile __attribute__((address_space(3))) int* slot = (volatile __attribute__((address_space(3))) int*)((__attribute__((address_space(3))) unsigned char*)lds + 131072 + 320 + 11000);
;     unsigned* q = (unsigned*)(P.ws + WS_CTL) + CW_DEFQ;
;     for (int n = 0; n < quota; ++n) {
;         __syncthreads();
;         if (tid == 0) *slot = (int)atomicAdd(q, 1u);
;         __syncthreads();
;         const int t = *slot;
;         if (t >= DEF_GU + DEF_DN) break;
;         const bool gu = t < DEF_GU;
;         const float* src = gu ? P.in[34] : P.in[36]; bf16* dst = (bf16*)(P.ws + (gu ? WS_WGU : WS_WDN));
;         const int N = gu ? 2048 : 1024, ntn = N / 256, it = gu ? 2 * NE * 16 * 8 - DEF_GU + t : 2 * NE * 16 * 4 - DEF_DN + (t - DEF_GU);
; __global__ void __launch_bounds__(NT, 2) mega(Args args) {
;     ...
;         g8::gemm_phase<g8::EpiStoreBf16, g8::DenseOrder, false, true>(LDSP, D, D, S, E);
;         if (IDLE_LAST(68 * 7)) convert_deferred(P, lds, 4); } SEAM(2);
.LBB0_779:
	s_abs_i32 s3, s62
	v_cvt_f32_u32_e32 v2, s3
	s_sub_i32 s4, 0, s3
	s_mov_b32 s5, 0
	v_rcp_iflag_f32_e32 v2, v2
	s_nop 0
	v_mul_f32_e32 v2, 0x4f7ffffe, v2
	v_cvt_u32_f32_e32 v2, v2
	s_nop 0
	v_readfirstlane_b32 s6, v2
	s_mul_i32 s4, s4, s6
	s_mul_hi_u32 s4, s6, s4
	s_add_i32 s6, s6, s4
	s_mul_hi_u32 s4, s6, 0x1dc
	s_mul_i32 s4, s4, s3
	s_sub_i32 s4, 0x1dc, s4
	s_sub_i32 s6, s4, s3
	s_cmp_ge_u32 s4, s3
	s_cselect_b32 s4, s6, s4
	s_sub_i32 s6, s4, s3
	s_cmp_ge_u32 s4, s3
	s_cselect_b32 s3, s6, s4
	s_cmp_eq_u32 s3, 0
	s_cselect_b64 s[6:7], -1, 0
	s_cmp_lt_i32 s2, s3
	s_cselect_b64 s[8:9], -1, 0
	s_or_b64 s[6:7], s[6:7], s[8:9]
	s_and_b64 vcc, exec, s[6:7]
	s_cbranch_vccnz .LBB0_789
	v_and_b32_e32 v2, 0x7c, v155
	v_lshlrev_b32_e32 v3, 5, v0
	s_movk_i32 s3, 0x400
	v_lshrrev_b32_e32 v4, 6, v0
	v_and_or_b32 v12, v3, s3, v2
	v_bfe_u32 v2, v0, 3, 3
	v_lshl_or_b32 v5, v4, 5, v2
	v_lshlrev_b32_e32 v2, 3, v0
	v_lshl_add_u32 v11, v182, 4, 0
	v_and_b32_e32 v2, 56, v2
	v_mul_u32_u24_e32 v16, 0x2020, v4
	v_mov_b32_e32 v3, 0
	v_lshl_add_u32 v27, v5, 2, 0
	v_mul_u32_u24_e32 v28, 0x404, v2
	v_lshlrev_b32_e32 v10, 6, v5
	s_add_i32 s12, 0, 0x22c38
	v_add_u32_e32 v16, v11, v16
	v_and_b32_e32 v13, 0xfc, v155
	v_and_b32_e32 v14, 56, v154
	s_mov_b32 s3, 4
	v_or_b32_e32 v4, 0x200, v10
	v_mov_b32_e32 v5, v3
	v_or_b32_e32 v6, 0x400, v10
	v_mov_b32_e32 v7, v3
	v_or_b32_e32 v8, 0x600, v10
	v_mov_b32_e32 v9, v3
	v_mov_b32_e32 v15, s12
	s_movk_i32 s13, 0x833
	s_movk_i32 s14, 0x800
	s_mov_b32 s15, 0x1104e000
	s_movk_i32 s16, 0x7cc
	v_add_u32_e32 v17, 0x404, v16
	v_add_u32_e32 v18, 0x40c, v16
	v_add_u32_e32 v19, 0x808, v16
	v_add_u32_e32 v20, 0xc0c, v16
	v_add_u32_e32 v21, 0xc14, v16
	v_add_u32_e32 v22, 0x1414, v16
	v_add_u32_e32 v23, 0x141c, v16
	v_add_u32_e32 v24, 0x1818, v16
	v_add_u32_e32 v25, 0x1c1c, v16
	v_add_u32_e32 v26, 0x1c24, v16
	v_lshlrev_b32_e32 v2, 1, v2
	v_add_u32_e32 v27, v27, v28
	v_lshlrev_b32_e32 v10, 1, v10
	s_branch .LBB0_782

; __device__ __forceinline__ unsigned g8_cvt_pk(float lo, float hi) { unsigned r; asm volatile("v_cvt_pk_bf16_f32 %0, %1, %2" : "=v"(r) : "v"(lo), "v"(hi)); return r; }
; __device__ __forceinline__ void convert_deferred(const Ptrs& P, unsigned char* lds, int quota) {
;     ...
;     for (int n = 0; n < quota; ++n) {
;         __syncthreads();
;         if (tid == 0) *slot = (int)atomicAdd(q, 1u);
;         __syncthreads();
;         const int t = *slot;
;         if (t >= DEF_GU + DEF_DN) break;
;         const bool gu = t < DEF_GU;
;         const float* src = gu ? P.in[34] : P.in[36]; bf16* dst = (bf16*)(P.ws + (gu ? WS_WGU : WS_WDN));
;         const int N = gu ? 2048 : 1024, ntn = N / 256, it = gu ? 2 * NE * 16 * 8 - DEF_GU + t : 2 * NE * 16 * 4 - DEF_DN + (t - DEF_GU);
;         f32x4 cur[8];
;         bt_load(src, N, gu ? 1 : 0, it, ntn, cur);
; #pragma unroll
;         for (int i = 0; i < 8; ++i) { float* tp = tile + (wid * 8 + i) * 257 + lane * 4; tp[0] = cur[i][0]; tp[1] = cur[i][1]; tp[2] = cur[i][2]; tp[3] = cur[i][3]; }
;         __syncthreads();
;         const int per = 16 * ntn, z = it / per, r = it % per, kt = r / ntn, nt = r % ntn;
;         bf16* d = dst + (size_t)z * N * 1024 + (((size_t)nt * 16 + kt) << 14);
;         const int kc = lane & 7;
; #pragma unroll
;         for (int pss = 0; pss < 4; ++pss) {
;             const int nn = wid * 32 + pss * 8 + (lane >> 3); float f[8];
; #pragma unroll
;             for (int j = 0; j < 8; ++j) f[j] = tile[(kc * 8 + j) * 257 + nn];
;             u32x4 w; w.x = g8_cvt_pk(f[0], f[1]); w.y = g8_cvt_pk(f[2], f[3]); w.z = g8_cvt_pk(f[4], f[5]); w.w = g8_cvt_pk(f[6], f[7]);
;             *(u32x4*)(d + nn * 64 + kc * 8) = w;
;         }
.LBB0_786:
	s_or_b64 exec, exec, s[6:7]
	s_waitcnt lgkmcnt(0)
	s_barrier
	ds_read_b32 v11, v15
	s_mov_b64 s[6:7], -1
	s_waitcnt lgkmcnt(0)
	v_cmp_lt_i32_e32 vcc, s13, v11
	v_readfirstlane_b32 s4, v11
	s_cbranch_vccnz .LBB0_781
	s_cmpk_gt_i32 s4, 0x577
	s_cselect_b64 vcc, -1, 0
	s_and_b64 s[6:7], vcc, exec
	s_cselect_b32 s6, s15, 0x104e000
	s_cselect_b32 s11, 0x400, s14
	s_cselect_b32 s17, s73, s69
	s_cselect_b32 s20, s72, s68
	s_cselect_b32 s7, s16, 0x1a88
	s_cselect_b32 s18, 20, 21
	s_cselect_b32 s21, 10, 11
	s_add_u32 s26, s78, s6
	s_addc_u32 s27, s79, 0
	s_lshr_b32 s8, s11, 4
	s_abs_i32 s6, s8
	v_cvt_f32_u32_e32 v11, s6
	s_sub_i32 s19, 0, s6
	s_add_i32 s7, s7, s4
	s_abs_i32 s9, s7
	v_rcp_iflag_f32_e32 v11, v11
	s_xor_b32 s4, s7, s8
	s_lshr_b32 s10, s11, 8
	s_ashr_i32 s4, s4, 31
	v_mul_f32_e32 v11, 0x4f7ffffe, v11
	v_cvt_u32_f32_e32 v11, v11
	s_nop 0
	v_readfirstlane_b32 s28, v11
	s_mul_i32 s19, s19, s28
	s_mul_hi_u32 s19, s28, s19
	s_add_i32 s28, s28, s19
	s_mul_hi_u32 s19, s9, s28
	s_mul_i32 s28, s19, s6
	s_sub_i32 s9, s9, s28
	s_add_i32 s28, s19, 1
	s_sub_i32 s29, s9, s6
	s_cmp_ge_u32 s9, s6
	s_cselect_b32 s19, s28, s19
	s_cselect_b32 s9, s29, s9
	s_add_i32 s28, s19, 1
	s_cmp_ge_u32 s9, s6
	s_cselect_b32 s6, s28, s19
	s_xor_b32 s6, s6, s4
	s_sub_i32 s6, s6, s4
	s_sext_i32_i8 s4, s10
	v_cvt_f32_i32_e32 v11, s4
	s_mul_i32 s8, s6, s8
	s_sub_i32 s7, s7, s8
	v_cvt_f32_i32_e32 v28, s7
	v_rcp_iflag_f32_e32 v29, v11
	s_xor_b32 s4, s7, s4
	s_ashr_i32 s4, s4, 30
	s_or_b32 s4, s4, 1
	v_mul_f32_e32 v29, v28, v29
	v_trunc_f32_e32 v29, v29
	v_fma_f32 v28, -v29, v11, v28
	v_cvt_i32_f32_e32 v29, v29
	v_cmp_ge_f32_e64 s[8:9], |v28|, |v11|
	s_and_b64 s[8:9], s[8:9], exec
	s_cselect_b32 s4, s4, 0
	v_readfirstlane_b32 s8, v29
	s_add_i32 s8, s8, s4
	s_mul_i32 s9, s8, s10
	s_sub_i32 s10, s7, s9
	s_sext_i32_i8 s7, s10
	v_lshl_add_u32 v11, s7, 7, v12
	v_lshl_or_b32 v28, s7, 8, v13
	s_ashr_i32 s7, s6, 31
	s_sext_i32_i8 s4, s8
	s_lshl_b64 s[18:19], s[6:7], s18
	v_lshl_or_b32 v30, s4, 6, v14
	s_lshl_b64 s[18:19], s[18:19], 2
	v_ashrrev_i32_e32 v31, 31, v30
	s_add_u32 s18, s20, s18
	v_cndmask_b32_e32 v28, v11, v28, vcc
	s_addc_u32 s19, s17, s19
	v_lshlrev_b64 v[30:31], s21, v[30:31]
	v_lshl_add_u64 v[30:31], v[30:31], 2, s[18:19]
	v_ashrrev_i32_e32 v29, 31, v28
	v_lshl_add_u64 v[52:53], v[28:29], 2, v[30:31]
	s_lshl_b64 s[18:19], 12, s21
	s_lshl_b32 s4, s11, 2
	v_lshl_add_u64 v[40:41], v[52:53], 0, s[18:19]
	s_lshl_b64 s[18:19], 24, s21
	v_lshl_add_u64 v[36:37], v[52:53], 0, s[4:5]
	v_lshl_add_u64 v[44:45], v[52:53], 0, s[18:19]
	s_lshl_b64 s[18:19], 28, s21
	v_lshl_add_u64 v[54:55], v[36:37], 0, s[4:5]
	v_lshl_add_u64 v[48:49], v[52:53], 0, s[18:19]
	s_lshl_b32 s4, s11, 3
	s_lshl_b64 s[18:19], 20, s21
	global_load_dwordx4 v[28:31], v[52:53], off nt
	global_load_dwordx4 v[32:35], v[36:37], off nt
	s_nop 0
	global_load_dwordx4 v[36:39], v[54:55], off nt
	s_nop 0
	global_load_dwordx4 v[40:43], v[40:41], off nt
	v_lshl_add_u64 v[54:55], v[54:55], 0, s[4:5]
	v_lshl_add_u64 v[56:57], v[52:53], 0, s[18:19]
	global_load_dwordx4 v[44:47], v[44:45], off nt
	s_nop 0
	global_load_dwordx4 v[48:51], v[48:49], off nt
	s_nop 0
	global_load_dwordx4 v[52:55], v[54:55], off nt
	s_nop 0
	global_load_dwordx4 v[56:59], v[56:57], off nt
	s_lshl_b64 s[6:7], s[6:7], s21
	s_lshl_b64 s[6:7], s[6:7], 11
	s_add_u32 s4, s26, s6
	s_addc_u32 s11, s27, s7
	s_bfe_i64 s[6:7], s[10:11], 0x80000
	s_bfe_i64 s[8:9], s[8:9], 0x80000
	s_lshl_b64 s[6:7], s[6:7], 19
	s_add_u32 s4, s4, s6
	s_addc_u32 s10, s11, s7
	s_lshl_b64 s[6:7], s[8:9], 15
	s_add_u32 s6, s4, s6
	s_addc_u32 s7, s10, s7
	v_mov_b32_e32 v11, v3
	s_add_i32 s3, s3, -1
	s_cmp_eq_u32 s3, 0
	s_waitcnt vmcnt(7)
	ds_write_b128 v16, v[28:31]
	s_waitcnt vmcnt(6)
	ds_write2_b32 v17, v32, v33 offset1:1
	ds_write2_b32 v18, v34, v35 offset1:1
	s_waitcnt vmcnt(3)
	ds_write2_b64 v24, v[44:45], v[46:47] offset1:1
	s_waitcnt vmcnt(2)
	ds_write2_b32 v25, v48, v49 offset1:1
	ds_write2_b32 v26, v50, v51 offset1:1
	ds_write2_b64 v19, v[36:37], v[38:39] offset1:1
	ds_write2_b32 v20, v40, v41 offset1:1
	ds_write2_b32 v21, v42, v43 offset1:1
	s_waitcnt vmcnt(1)
	ds_write_b128 v16, v[52:55] offset:4112
	s_waitcnt vmcnt(0)
	ds_write2_b32 v22, v56, v57 offset1:1
	ds_write2_b32 v23, v58, v59 offset1:1
	s_waitcnt lgkmcnt(0)
	s_barrier
	ds_read_b32 v28, v27 offset:1028
	ds_read_b32 v29, v27 offset:3084
	ds_read_b32 v30, v27 offset:5140
	ds_read_b32 v31, v27 offset:7196
	ds_read_b32 v32, v27 offset:6168
	ds_read_b32 v33, v27 offset:4112
	ds_read_b32 v34, v27 offset:2056
	ds_read_b32 v35, v27
	s_waitcnt lgkmcnt(0)
	v_cvt_pk_bf16_f32 v28, v35, v28
	v_cvt_pk_bf16_f32 v29, v34, v29
	v_cvt_pk_bf16_f32 v30, v33, v30
	v_cvt_pk_bf16_f32 v31, v32, v31
	ds_read_b32 v36, v27 offset:1060
	ds_read_b32 v37, v27 offset:3116
	ds_read_b32 v38, v27 offset:5172
	ds_read_b32 v39, v27 offset:7228
	ds_read_b32 v40, v27 offset:6200
	ds_read_b32 v41, v27 offset:4144
	ds_read_b32 v42, v27 offset:2088
	ds_read_b32 v43, v27 offset:32
	v_lshl_add_u64 v[32:33], s[6:7], 0, v[2:3]
	v_lshl_add_u64 v[34:35], v[32:33], 0, v[10:11]
	global_store_dwordx4 v[34:35], v[28:31], off
	v_lshl_add_u64 v[34:35], v[4:5], 1, v[32:33]
	s_cselect_b64 s[6:7], -1, 0
	s_waitcnt lgkmcnt(0)
	v_cvt_pk_bf16_f32 v28, v43, v36
	v_cvt_pk_bf16_f32 v29, v42, v37
	v_cvt_pk_bf16_f32 v30, v41, v38
	v_cvt_pk_bf16_f32 v31, v40, v39
	ds_read_b32 v11, v27 offset:1092
	ds_read_b32 v36, v27 offset:3148
	ds_read_b32 v37, v27 offset:6232
	ds_read_b32 v38, v27 offset:4176
	ds_read_b32 v39, v27 offset:2120
	ds_read_b32 v40, v27 offset:64
	ds_read_b32 v41, v27 offset:5204
	ds_read_b32 v42, v27 offset:7260
	global_store_dwordx4 v[34:35], v[28:31], off
	v_lshl_add_u64 v[34:35], v[6:7], 1, v[32:33]
	v_lshl_add_u64 v[32:33], v[8:9], 1, v[32:33]
	s_waitcnt lgkmcnt(2)
	v_cvt_pk_bf16_f32 v28, v40, v11
	v_cvt_pk_bf16_f32 v29, v39, v36
	s_waitcnt lgkmcnt(1)
	v_cvt_pk_bf16_f32 v30, v38, v41
	s_waitcnt lgkmcnt(0)
	v_cvt_pk_bf16_f32 v31, v37, v42
	ds_read_b32 v11, v27 offset:1124
	ds_read_b32 v36, v27 offset:3180
	ds_read_b32 v37, v27 offset:6264
	ds_read_b32 v38, v27 offset:4208
	ds_read_b32 v39, v27 offset:2152
	ds_read_b32 v40, v27 offset:96
	ds_read_b32 v41, v27 offset:5236
	ds_read_b32 v42, v27 offset:7292
	global_store_dwordx4 v[34:35], v[28:31], off
	s_waitcnt lgkmcnt(2)
	s_nop 0
	v_cvt_pk_bf16_f32 v28, v40, v11
	v_cvt_pk_bf16_f32 v29, v39, v36
	s_waitcnt lgkmcnt(1)
	v_cvt_pk_bf16_f32 v30, v38, v41
	s_waitcnt lgkmcnt(0)
	v_cvt_pk_bf16_f32 v31, v37, v42
	global_store_dwordx4 v[32:33], v[28:31], off
	s_branch .LBB0_781

; #define SEAM(k) do { if (IN(k) && IN((k) + 1)) xcd_barrier(bar); \
;         if (PROBE_MASK) { const unsigned long long t_ = __builtin_amdgcn_s_memrealtime(); if ((PROBE_MASK >> (k)) & 1u) pr_acc += t_ - pr_t0; pr_t0 = t_; } } while (0)
; __device__ __forceinline__ void convert_deferred(const Ptrs& P, unsigned char* lds, int quota) {
;     const int tid = threadIdx.x, wid = tid >> 6, lane = tid & 63;
;     float* tile = (float*)lds;
;     volatile __attribute__((address_space(3))) int* slot = (volatile __attribute__((address_space(3))) int*)((__attribute__((address_space(3))) unsigned char*)lds + 131072 + 320 + 11000);
;     unsigned* q = (unsigned*)(P.ws + WS_CTL) + CW_DEFQ;
;     for (int n = 0; n < quota; ++n) {
;         __syncthreads();
;         if (tid == 0) *slot = (int)atomicAdd(q, 1u);
;         __syncthreads();
;         const int t = *slot;
;         if (t >= DEF_GU + DEF_DN) break;
;         const bool gu = t < DEF_GU;
;         const float* src = gu ? P.in[34] : P.in[36]; bf16* dst = (bf16*)(P.ws + (gu ? WS_WGU : WS_WDN));
;         const int N = gu ? 2048 : 1024, ntn = N / 256, it = gu ? 2 * NE * 16 * 8 - DEF_GU + t : 2 * NE * 16 * 4 - DEF_DN + (t - DEF_GU);
; __global__ void __launch_bounds__(NT, 2) mega(Args args) {
;     ...
;         g8::gemm_phase<g8::EpiOut, g8::DenseOrder, false, true>(LDSP, D, D, S, E);
;         if (IDLE_LAST(68 * 4)) convert_deferred(P, lds, 4); } SEAM(6);
.LBB0_1286:
	s_abs_i32 s3, s62
	v_cvt_f32_u32_e32 v2, s3
	s_sub_i32 s4, 0, s3
	s_mov_b32 s5, 0
	v_rcp_iflag_f32_e32 v2, v2
	s_nop 0
	v_mul_f32_e32 v2, 0x4f7ffffe, v2
	v_cvt_u32_f32_e32 v2, v2
	s_nop 0
	v_readfirstlane_b32 s6, v2
	s_mul_i32 s4, s4, s6
	s_mul_hi_u32 s4, s6, s4
	s_add_i32 s6, s6, s4
	s_mul_hi_u32 s4, s6, 0x110
	s_mul_i32 s4, s4, s3
	s_sub_i32 s4, 0x110, s4
	s_sub_i32 s6, s4, s3
	s_cmp_ge_u32 s4, s3
	s_cselect_b32 s4, s6, s4
	s_sub_i32 s6, s4, s3
	s_cmp_ge_u32 s4, s3
	s_cselect_b32 s3, s6, s4
	s_cmp_eq_u32 s3, 0
	s_cselect_b64 s[6:7], -1, 0
	s_cmp_lt_i32 s2, s3
	s_cselect_b64 s[8:9], -1, 0
	s_or_b64 s[6:7], s[6:7], s[8:9]
	s_and_b64 vcc, exec, s[6:7]
	s_cbranch_vccnz .LBB0_1296
	v_and_b32_e32 v2, 0x7c, v188
	v_lshlrev_b32_e32 v3, 5, v0
	s_movk_i32 s3, 0x400
	v_and_or_b32 v12, v3, s3, v2
	v_bfe_u32 v2, v0, 3, 3
	v_lshl_or_b32 v4, v1, 5, v2
	v_lshlrev_b32_e32 v2, 3, v0
	v_lshl_add_u32 v11, v182, 4, 0
	v_and_b32_e32 v2, 56, v2
	v_mul_u32_u24_e32 v16, 0x2020, v1
	v_mov_b32_e32 v3, 0
	v_lshl_add_u32 v27, v4, 2, 0
	v_mul_u32_u24_e32 v28, 0x404, v2
	v_lshlrev_b32_e32 v10, 6, v4
	s_add_i32 s12, 0, 0x22c38
	v_add_u32_e32 v16, v11, v16
	v_and_b32_e32 v13, 0xfc, v188
	v_and_b32_e32 v14, 56, v185
	s_mov_b32 s3, 4
	v_or_b32_e32 v4, 0x200, v10
	v_mov_b32_e32 v5, v3
	v_or_b32_e32 v6, 0x400, v10
	v_mov_b32_e32 v7, v3
	v_or_b32_e32 v8, 0x600, v10
	v_mov_b32_e32 v9, v3
	v_mov_b32_e32 v15, s12
	s_movk_i32 s13, 0x833
	s_movk_i32 s14, 0x800
	s_mov_b32 s15, 0x1104e000
	s_movk_i32 s16, 0x7cc
	v_add_u32_e32 v17, 0x404, v16
	v_add_u32_e32 v18, 0x40c, v16
	v_add_u32_e32 v19, 0x808, v16
	v_add_u32_e32 v20, 0xc0c, v16
	v_add_u32_e32 v21, 0xc14, v16
	v_add_u32_e32 v22, 0x1414, v16
	v_add_u32_e32 v23, 0x141c, v16
	v_add_u32_e32 v24, 0x1818, v16
	v_add_u32_e32 v25, 0x1c1c, v16
	v_add_u32_e32 v26, 0x1c24, v16
	v_lshlrev_b32_e32 v2, 1, v2
	v_add_u32_e32 v27, v27, v28
	v_lshlrev_b32_e32 v10, 1, v10
	s_branch .LBB0_1289

; __device__ __forceinline__ unsigned g8_cvt_pk(float lo, float hi) { unsigned r; asm volatile("v_cvt_pk_bf16_f32 %0, %1, %2" : "=v"(r) : "v"(lo), "v"(hi)); return r; }
; __device__ __forceinline__ void convert_deferred(const Ptrs& P, unsigned char* lds, int quota) {
;     ...
;     for (int n = 0; n < quota; ++n) {
;         __syncthreads();
;         if (tid == 0) *slot = (int)atomicAdd(q, 1u);
;         __syncthreads();
;         const int t = *slot;
;         if (t >= DEF_GU + DEF_DN) break;
;         const bool gu = t < DEF_GU;
;         const float* src = gu ? P.in[34] : P.in[36]; bf16* dst = (bf16*)(P.ws + (gu ? WS_WGU : WS_WDN));
;         const int N = gu ? 2048 : 1024, ntn = N / 256, it = gu ? 2 * NE * 16 * 8 - DEF_GU + t : 2 * NE * 16 * 4 - DEF_DN + (t - DEF_GU);
;         f32x4 cur[8];
;         bt_load(src, N, gu ? 1 : 0, it, ntn, cur);
; #pragma unroll
;         for (int i = 0; i < 8; ++i) { float* tp = tile + (wid * 8 + i) * 257 + lane * 4; tp[0] = cur[i][0]; tp[1] = cur[i][1]; tp[2] = cur[i][2]; tp[3] = cur[i][3]; }
;         __syncthreads();
;         const int per = 16 * ntn, z = it / per, r = it % per, kt = r / ntn, nt = r % ntn;
;         bf16* d = dst + (size_t)z * N * 1024 + (((size_t)nt * 16 + kt) << 14);
;         const int kc = lane & 7;
; #pragma unroll
;         for (int pss = 0; pss < 4; ++pss) {
;             const int nn = wid * 32 + pss * 8 + (lane >> 3); float f[8];
; #pragma unroll
;             for (int j = 0; j < 8; ++j) f[j] = tile[(kc * 8 + j) * 257 + nn];
;             u32x4 w; w.x = g8_cvt_pk(f[0], f[1]); w.y = g8_cvt_pk(f[2], f[3]); w.z = g8_cvt_pk(f[4], f[5]); w.w = g8_cvt_pk(f[6], f[7]);
;             *(u32x4*)(d + nn * 64 + kc * 8) = w;
;         }
.LBB0_1293:
	s_or_b64 exec, exec, s[6:7]
	s_waitcnt lgkmcnt(0)
	s_barrier
	ds_read_b32 v11, v15
	s_mov_b64 s[6:7], -1
	s_waitcnt lgkmcnt(0)
	v_cmp_lt_i32_e32 vcc, s13, v11
	v_readfirstlane_b32 s4, v11
	s_cbranch_vccnz .LBB0_1288
	s_cmpk_gt_i32 s4, 0x577
	s_cselect_b64 vcc, -1, 0
	s_and_b64 s[6:7], vcc, exec
	s_cselect_b32 s6, s15, 0x104e000
	s_cselect_b32 s11, 0x400, s14
	s_cselect_b32 s17, s73, s69
	s_cselect_b32 s20, s72, s68
	s_cselect_b32 s7, s16, 0x1a88
	s_cselect_b32 s18, 20, 21
	s_cselect_b32 s21, 10, 11
	s_add_u32 s22, s78, s6
	s_addc_u32 s23, s79, 0
	s_lshr_b32 s8, s11, 4
	s_abs_i32 s6, s8
	v_cvt_f32_u32_e32 v11, s6
	s_sub_i32 s19, 0, s6
	s_add_i32 s7, s7, s4
	s_abs_i32 s9, s7
	v_rcp_iflag_f32_e32 v11, v11
	s_xor_b32 s4, s7, s8
	s_lshr_b32 s10, s11, 8
	s_ashr_i32 s4, s4, 31
	v_mul_f32_e32 v11, 0x4f7ffffe, v11
	v_cvt_u32_f32_e32 v11, v11
	s_nop 0
	v_readfirstlane_b32 s24, v11
	s_mul_i32 s19, s19, s24
	s_mul_hi_u32 s19, s24, s19
	s_add_i32 s24, s24, s19
	s_mul_hi_u32 s19, s9, s24
	s_mul_i32 s24, s19, s6
	s_sub_i32 s9, s9, s24
	s_add_i32 s24, s19, 1
	s_sub_i32 s25, s9, s6
	s_cmp_ge_u32 s9, s6
	s_cselect_b32 s19, s24, s19
	s_cselect_b32 s9, s25, s9
	s_add_i32 s24, s19, 1
	s_cmp_ge_u32 s9, s6
	s_cselect_b32 s6, s24, s19
	s_xor_b32 s6, s6, s4
	s_sub_i32 s6, s6, s4
	s_sext_i32_i8 s4, s10
	v_cvt_f32_i32_e32 v11, s4
	s_mul_i32 s8, s6, s8
	s_sub_i32 s7, s7, s8
	v_cvt_f32_i32_e32 v28, s7
	v_rcp_iflag_f32_e32 v29, v11
	s_xor_b32 s4, s7, s4
	s_ashr_i32 s4, s4, 30
	s_or_b32 s4, s4, 1
	v_mul_f32_e32 v29, v28, v29
	v_trunc_f32_e32 v29, v29
	v_fma_f32 v28, -v29, v11, v28
	v_cvt_i32_f32_e32 v29, v29
	v_cmp_ge_f32_e64 s[8:9], |v28|, |v11|
	s_and_b64 s[8:9], s[8:9], exec
	s_cselect_b32 s4, s4, 0
	v_readfirstlane_b32 s8, v29
	s_add_i32 s8, s8, s4
	s_mul_i32 s9, s8, s10
	s_sub_i32 s10, s7, s9
	s_sext_i32_i8 s7, s10
	v_lshl_add_u32 v11, s7, 7, v12
	v_lshl_or_b32 v28, s7, 8, v13
	s_ashr_i32 s7, s6, 31
	s_sext_i32_i8 s4, s8
	s_lshl_b64 s[18:19], s[6:7], s18
	v_lshl_or_b32 v30, s4, 6, v14
	s_lshl_b64 s[18:19], s[18:19], 2
	v_ashrrev_i32_e32 v31, 31, v30
	s_add_u32 s18, s20, s18
	v_cndmask_b32_e32 v28, v11, v28, vcc
	s_addc_u32 s19, s17, s19
	v_lshlrev_b64 v[30:31], s21, v[30:31]
	v_lshl_add_u64 v[30:31], v[30:31], 2, s[18:19]
	v_ashrrev_i32_e32 v29, 31, v28
	v_lshl_add_u64 v[52:53], v[28:29], 2, v[30:31]
	s_lshl_b64 s[18:19], 12, s21
	s_lshl_b32 s4, s11, 2
	v_lshl_add_u64 v[40:41], v[52:53], 0, s[18:19]
	s_lshl_b64 s[18:19], 24, s21
	v_lshl_add_u64 v[36:37], v[52:53], 0, s[4:5]
	v_lshl_add_u64 v[44:45], v[52:53], 0, s[18:19]
	s_lshl_b64 s[18:19], 28, s21
	v_lshl_add_u64 v[54:55], v[36:37], 0, s[4:5]
	v_lshl_add_u64 v[48:49], v[52:53], 0, s[18:19]
	s_lshl_b32 s4, s11, 3
	s_lshl_b64 s[18:19], 20, s21
	global_load_dwordx4 v[28:31], v[52:53], off nt
	global_load_dwordx4 v[32:35], v[36:37], off nt
	s_nop 0
	global_load_dwordx4 v[36:39], v[54:55], off nt
	s_nop 0
	global_load_dwordx4 v[40:43], v[40:41], off nt
	v_lshl_add_u64 v[54:55], v[54:55], 0, s[4:5]
	v_lshl_add_u64 v[56:57], v[52:53], 0, s[18:19]
	global_load_dwordx4 v[44:47], v[44:45], off nt
	s_nop 0
	global_load_dwordx4 v[48:51], v[48:49], off nt
	s_nop 0
	global_load_dwordx4 v[52:55], v[54:55], off nt
	s_nop 0
	global_load_dwordx4 v[56:59], v[56:57], off nt
	s_lshl_b64 s[6:7], s[6:7], s21
	s_lshl_b64 s[6:7], s[6:7], 11
	s_add_u32 s4, s22, s6
	s_addc_u32 s11, s23, s7
	s_bfe_i64 s[6:7], s[10:11], 0x80000
	s_bfe_i64 s[8:9], s[8:9], 0x80000
	s_lshl_b64 s[6:7], s[6:7], 19
	s_add_u32 s4, s4, s6
	s_addc_u32 s10, s11, s7
	s_lshl_b64 s[6:7], s[8:9], 15
	s_add_u32 s6, s4, s6
	s_addc_u32 s7, s10, s7
	v_mov_b32_e32 v11, v3
	s_add_i32 s3, s3, -1
	s_cmp_eq_u32 s3, 0
	s_waitcnt vmcnt(7)
	ds_write_b128 v16, v[28:31]
	s_waitcnt vmcnt(6)
	ds_write2_b32 v17, v32, v33 offset1:1
	ds_write2_b32 v18, v34, v35 offset1:1
	s_waitcnt vmcnt(3)
	ds_write2_b64 v24, v[44:45], v[46:47] offset1:1
	s_waitcnt vmcnt(2)
	ds_write2_b32 v25, v48, v49 offset1:1
	ds_write2_b32 v26, v50, v51 offset1:1
	ds_write2_b64 v19, v[36:37], v[38:39] offset1:1
	ds_write2_b32 v20, v40, v41 offset1:1
	ds_write2_b32 v21, v42, v43 offset1:1
	s_waitcnt vmcnt(1)
	ds_write_b128 v16, v[52:55] offset:4112
	s_waitcnt vmcnt(0)
	ds_write2_b32 v22, v56, v57 offset1:1
	ds_write2_b32 v23, v58, v59 offset1:1
	s_waitcnt lgkmcnt(0)
	s_barrier
	ds_read_b32 v28, v27 offset:1028
	ds_read_b32 v29, v27 offset:3084
	ds_read_b32 v30, v27 offset:5140
	ds_read_b32 v31, v27 offset:7196
	ds_read_b32 v32, v27 offset:6168
	ds_read_b32 v33, v27 offset:4112
	ds_read_b32 v34, v27 offset:2056
	ds_read_b32 v35, v27
	s_waitcnt lgkmcnt(0)
	v_cvt_pk_bf16_f32 v28, v35, v28
	v_cvt_pk_bf16_f32 v29, v34, v29
	v_cvt_pk_bf16_f32 v30, v33, v30
	v_cvt_pk_bf16_f32 v31, v32, v31
	ds_read_b32 v36, v27 offset:1060
	ds_read_b32 v37, v27 offset:3116
	ds_read_b32 v38, v27 offset:5172
	ds_read_b32 v39, v27 offset:7228
	ds_read_b32 v40, v27 offset:6200
	ds_read_b32 v41, v27 offset:4144
	ds_read_b32 v42, v27 offset:2088
	ds_read_b32 v43, v27 offset:32
	v_lshl_add_u64 v[32:33], s[6:7], 0, v[2:3]
	v_lshl_add_u64 v[34:35], v[32:33], 0, v[10:11]
	global_store_dwordx4 v[34:35], v[28:31], off
	v_lshl_add_u64 v[34:35], v[4:5], 1, v[32:33]
	s_cselect_b64 s[6:7], -1, 0
	s_waitcnt lgkmcnt(0)
	v_cvt_pk_bf16_f32 v28, v43, v36
	v_cvt_pk_bf16_f32 v29, v42, v37
	v_cvt_pk_bf16_f32 v30, v41, v38
	v_cvt_pk_bf16_f32 v31, v40, v39
	ds_read_b32 v11, v27 offset:1092
	ds_read_b32 v36, v27 offset:3148
	ds_read_b32 v37, v27 offset:6232
	ds_read_b32 v38, v27 offset:4176
	ds_read_b32 v39, v27 offset:2120
	ds_read_b32 v40, v27 offset:64
	ds_read_b32 v41, v27 offset:5204
	ds_read_b32 v42, v27 offset:7260
	global_store_dwordx4 v[34:35], v[28:31], off
	v_lshl_add_u64 v[34:35], v[6:7], 1, v[32:33]
	v_lshl_add_u64 v[32:33], v[8:9], 1, v[32:33]
	s_waitcnt lgkmcnt(2)
	v_cvt_pk_bf16_f32 v28, v40, v11
	v_cvt_pk_bf16_f32 v29, v39, v36
	s_waitcnt lgkmcnt(1)
	v_cvt_pk_bf16_f32 v30, v38, v41
	s_waitcnt lgkmcnt(0)
	v_cvt_pk_bf16_f32 v31, v37, v42
	ds_read_b32 v11, v27 offset:1124
	ds_read_b32 v36, v27 offset:3180
	ds_read_b32 v37, v27 offset:6264
	ds_read_b32 v38, v27 offset:4208
	ds_read_b32 v39, v27 offset:2152
	ds_read_b32 v40, v27 offset:96
	ds_read_b32 v41, v27 offset:5236
	ds_read_b32 v42, v27 offset:7292
	global_store_dwordx4 v[34:35], v[28:31], off
	s_waitcnt lgkmcnt(2)
	s_nop 0
	v_cvt_pk_bf16_f32 v28, v40, v11
	v_cvt_pk_bf16_f32 v29, v39, v36
	s_waitcnt lgkmcnt(1)
	v_cvt_pk_bf16_f32 v30, v38, v41
	s_waitcnt lgkmcnt(0)
	v_cvt_pk_bf16_f32 v31, v37, v42
	global_store_dwordx4 v[32:33], v[28:31], off
	s_branch .LBB0_1288

; #define LAS __attribute__((address_space(3)))
; #define SEAM(k) do { if (IN(k) && IN((k) + 1)) xcd_barrier(bar); \
;         if (PROBE_MASK) { const unsigned long long t_ = __builtin_amdgcn_s_memrealtime(); if ((PROBE_MASK >> (k)) & 1u) pr_acc += t_ - pr_t0; pr_t0 = t_; } } while (0)
; __device__ __forceinline__ void convert_deferred(const Ptrs& P, unsigned char* lds, int quota) {
;     const int tid = threadIdx.x, wid = tid >> 6, lane = tid & 63;
;     float* tile = (float*)lds;
;     volatile __attribute__((address_space(3))) int* slot = (volatile __attribute__((address_space(3))) int*)((__attribute__((address_space(3))) unsigned char*)lds + 131072 + 320 + 11000);
;     unsigned* q = (unsigned*)(P.ws + WS_CTL) + CW_DEFQ;
;     for (int n = 0; n < quota; ++n) {
;         __syncthreads();
;         if (tid == 0) *slot = (int)atomicAdd(q, 1u);
;         __syncthreads();
;         const int t = *slot;
;         if (t >= DEF_GU + DEF_DN) break;
;         const bool gu = t < DEF_GU;
;         const float* src = gu ? P.in[34] : P.in[36]; bf16* dst = (bf16*)(P.ws + (gu ? WS_WGU : WS_WDN));
;         const int N = gu ? 2048 : 1024, ntn = N / 256, it = gu ? 2 * NE * 16 * 8 - DEF_GU + t : 2 * NE * 16 * 4 - DEF_DN + (t - DEF_GU);
; __global__ void __launch_bounds__(NT, 2) mega(Args args) {
;     ...
;         S.init((const unsigned*)(ws + WS_CTL) + CW_CNT + 0 * 64, (LAS int*)(LDSP + MISC_OFF + 256)); g8::EpiMoe2 E{P, 0}; g8::gemm_phase<g8::EpiMoe2, g8::MoeOrder, false, true>(LDSP, D, D, S, E);
;         { const int rem_ = ((LAS int*)(LDSP + MISC_OFF + 256))[96] % G; if (rem_ != 0 && vcu >= rem_) convert_deferred(P, lds, 5); } } SEAM(9);
.LBB0_1609:
	s_abs_i32 s0, s62
	v_cvt_f32_u32_e32 v2, s0
	s_sub_i32 s5, 0, s0
	s_abs_i32 s4, s9
	s_ashr_i32 s3, s9, 31
	v_rcp_iflag_f32_e32 v2, v2
	s_mov_b32 s1, 0
	v_mul_f32_e32 v2, 0x4f7ffffe, v2
	v_cvt_u32_f32_e32 v2, v2
	s_nop 0
	v_readfirstlane_b32 s6, v2
	s_mul_i32 s5, s5, s6
	s_mul_hi_u32 s5, s6, s5
	s_add_i32 s6, s6, s5
	s_mul_hi_u32 s5, s4, s6
	s_mul_i32 s5, s5, s0
	s_sub_i32 s4, s4, s5
	s_sub_i32 s5, s4, s0
	s_cmp_ge_u32 s4, s0
	s_cselect_b32 s4, s5, s4
	s_sub_i32 s5, s4, s0
	s_cmp_ge_u32 s4, s0
	s_cselect_b32 s0, s5, s4
	s_xor_b32 s0, s0, s3
	s_sub_i32 s0, s0, s3
	s_cmp_eq_u32 s0, 0
	v_readlane_b32 s3, v254, 2
	s_cselect_b64 s[4:5], -1, 0
	s_cmp_lt_i32 s3, s0
	s_cselect_b64 s[6:7], -1, 0
	s_or_b64 s[4:5], s[4:5], s[6:7]
	s_and_b64 vcc, exec, s[4:5]
	s_cbranch_vccnz .LBB0_1619
	v_and_b32_e32 v2, 0x7c, v175
	v_lshlrev_b32_e32 v3, 5, v0
	s_movk_i32 s0, 0x400
	v_and_or_b32 v12, v3, s0, v2
	v_bfe_u32 v2, v0, 3, 3
	v_lshl_or_b32 v4, v1, 5, v2
	v_lshlrev_b32_e32 v2, 3, v0
	v_lshl_add_u32 v11, v182, 4, 0
	v_and_b32_e32 v2, 56, v2
	v_mul_u32_u24_e32 v16, 0x2020, v1
	v_mov_b32_e32 v3, 0
	v_lshl_add_u32 v27, v4, 2, 0
	v_mul_u32_u24_e32 v28, 0x404, v2
	v_lshlrev_b32_e32 v10, 6, v4
	s_add_i32 s10, 0, 0x22c38
	v_add_u32_e32 v16, v11, v16
	s_mov_b32 s3, 5
	v_and_b32_e32 v13, 0xfc, v175
	v_and_b32_e32 v14, 56, v173
	v_or_b32_e32 v4, 0x200, v10
	v_mov_b32_e32 v5, v3
	v_or_b32_e32 v6, 0x400, v10
	v_mov_b32_e32 v7, v3
	v_or_b32_e32 v8, 0x600, v10
	v_mov_b32_e32 v9, v3
	v_mov_b32_e32 v15, s10
	s_movk_i32 s11, 0x833
	s_movk_i32 s12, 0x800
	s_mov_b32 s13, 0x1104e000
	s_movk_i32 s14, 0x7cc
	v_add_u32_e32 v17, 0x404, v16
	v_add_u32_e32 v18, 0x40c, v16
	v_add_u32_e32 v19, 0x808, v16
	v_add_u32_e32 v20, 0xc0c, v16
	v_add_u32_e32 v21, 0xc14, v16
	v_add_u32_e32 v22, 0x1414, v16
	v_add_u32_e32 v23, 0x141c, v16
	v_add_u32_e32 v24, 0x1818, v16
	v_add_u32_e32 v25, 0x1c1c, v16
	v_add_u32_e32 v26, 0x1c24, v16
	v_lshlrev_b32_e32 v2, 1, v2
	v_add_u32_e32 v27, v27, v28
	v_lshlrev_b32_e32 v10, 1, v10
	s_branch .LBB0_1612

; __device__ __forceinline__ unsigned g8_cvt_pk(float lo, float hi) { unsigned r; asm volatile("v_cvt_pk_bf16_f32 %0, %1, %2" : "=v"(r) : "v"(lo), "v"(hi)); return r; }
; __device__ __forceinline__ void convert_deferred(const Ptrs& P, unsigned char* lds, int quota) {
;     ...
;     for (int n = 0; n < quota; ++n) {
;         __syncthreads();
;         if (tid == 0) *slot = (int)atomicAdd(q, 1u);
;         __syncthreads();
;         const int t = *slot;
;         if (t >= DEF_GU + DEF_DN) break;
;         const bool gu = t < DEF_GU;
;         const float* src = gu ? P.in[34] : P.in[36]; bf16* dst = (bf16*)(P.ws + (gu ? WS_WGU : WS_WDN));
;         const int N = gu ? 2048 : 1024, ntn = N / 256, it = gu ? 2 * NE * 16 * 8 - DEF_GU + t : 2 * NE * 16 * 4 - DEF_DN + (t - DEF_GU);
;         f32x4 cur[8];
;         bt_load(src, N, gu ? 1 : 0, it, ntn, cur);
; #pragma unroll
;         for (int i = 0; i < 8; ++i) { float* tp = tile + (wid * 8 + i) * 257 + lane * 4; tp[0] = cur[i][0]; tp[1] = cur[i][1]; tp[2] = cur[i][2]; tp[3] = cur[i][3]; }
;         __syncthreads();
;         const int per = 16 * ntn, z = it / per, r = it % per, kt = r / ntn, nt = r % ntn;
;         bf16* d = dst + (size_t)z * N * 1024 + (((size_t)nt * 16 + kt) << 14);
;         const int kc = lane & 7;
; #pragma unroll
;         for (int pss = 0; pss < 4; ++pss) {
;             const int nn = wid * 32 + pss * 8 + (lane >> 3); float f[8];
; #pragma unroll
;             for (int j = 0; j < 8; ++j) f[j] = tile[(kc * 8 + j) * 257 + nn];
;             u32x4 w; w.x = g8_cvt_pk(f[0], f[1]); w.y = g8_cvt_pk(f[2], f[3]); w.z = g8_cvt_pk(f[4], f[5]); w.w = g8_cvt_pk(f[6], f[7]);
;             *(u32x4*)(d + nn * 64 + kc * 8) = w;
;         }
.LBB0_1616:
	s_or_b64 exec, exec, s[4:5]
	s_waitcnt lgkmcnt(0)
	s_barrier
	ds_read_b32 v11, v15
	s_mov_b64 s[4:5], -1
	s_waitcnt lgkmcnt(0)
	v_cmp_lt_i32_e32 vcc, s11, v11
	v_readfirstlane_b32 s0, v11
	s_cbranch_vccnz .LBB0_1611
	s_cmpk_gt_i32 s0, 0x577
	s_cselect_b64 vcc, -1, 0
	s_and_b64 s[4:5], vcc, exec
	s_cselect_b32 s4, s13, 0x104e000
	s_cselect_b32 s9, 0x400, s12
	s_cselect_b32 s15, s73, s69
	s_cselect_b32 s18, s72, s68
	s_cselect_b32 s5, s14, 0x1a88
	s_cselect_b32 s16, 20, 21
	s_cselect_b32 s19, 10, 11
	s_add_u32 s20, s78, s4
	s_addc_u32 s21, s79, 0
	s_lshr_b32 s6, s9, 4
	s_abs_i32 s4, s6
	v_cvt_f32_u32_e32 v11, s4
	s_sub_i32 s17, 0, s4
	s_add_i32 s5, s5, s0
	s_abs_i32 s7, s5
	v_rcp_iflag_f32_e32 v11, v11
	s_xor_b32 s0, s5, s6
	s_lshr_b32 s8, s9, 8
	s_ashr_i32 s0, s0, 31
	v_mul_f32_e32 v11, 0x4f7ffffe, v11
	v_cvt_u32_f32_e32 v11, v11
	s_nop 0
	v_readfirstlane_b32 s22, v11
	s_mul_i32 s17, s17, s22
	s_mul_hi_u32 s17, s22, s17
	s_add_i32 s22, s22, s17
	s_mul_hi_u32 s17, s7, s22
	s_mul_i32 s22, s17, s4
	s_sub_i32 s7, s7, s22
	s_add_i32 s22, s17, 1
	s_sub_i32 s23, s7, s4
	s_cmp_ge_u32 s7, s4
	s_cselect_b32 s17, s22, s17
	s_cselect_b32 s7, s23, s7
	s_add_i32 s22, s17, 1
	s_cmp_ge_u32 s7, s4
	s_cselect_b32 s4, s22, s17
	s_xor_b32 s4, s4, s0
	s_sub_i32 s4, s4, s0
	s_sext_i32_i8 s0, s8
	v_cvt_f32_i32_e32 v11, s0
	s_mul_i32 s6, s4, s6
	s_sub_i32 s5, s5, s6
	v_cvt_f32_i32_e32 v28, s5
	v_rcp_iflag_f32_e32 v29, v11
	s_xor_b32 s0, s5, s0
	s_ashr_i32 s0, s0, 30
	s_or_b32 s0, s0, 1
	v_mul_f32_e32 v29, v28, v29
	v_trunc_f32_e32 v29, v29
	v_fma_f32 v28, -v29, v11, v28
	v_cvt_i32_f32_e32 v29, v29
	v_cmp_ge_f32_e64 s[6:7], |v28|, |v11|
	s_and_b64 s[6:7], s[6:7], exec
	s_cselect_b32 s0, s0, 0
	v_readfirstlane_b32 s6, v29
	s_add_i32 s6, s6, s0
	s_mul_i32 s7, s6, s8
	s_sub_i32 s8, s5, s7
	s_sext_i32_i8 s5, s8
	v_lshl_add_u32 v11, s5, 7, v12
	v_lshl_or_b32 v28, s5, 8, v13
	s_ashr_i32 s5, s4, 31
	s_sext_i32_i8 s0, s6
	s_lshl_b64 s[16:17], s[4:5], s16
	v_lshl_or_b32 v30, s0, 6, v14
	s_lshl_b64 s[16:17], s[16:17], 2
	v_ashrrev_i32_e32 v31, 31, v30
	s_add_u32 s16, s18, s16
	v_cndmask_b32_e32 v28, v11, v28, vcc
	s_addc_u32 s17, s15, s17
	v_lshlrev_b64 v[30:31], s19, v[30:31]
	v_lshl_add_u64 v[30:31], v[30:31], 2, s[16:17]
	v_ashrrev_i32_e32 v29, 31, v28
	v_lshl_add_u64 v[52:53], v[28:29], 2, v[30:31]
	s_lshl_b64 s[16:17], 12, s19
	s_lshl_b32 s0, s9, 2
	v_lshl_add_u64 v[40:41], v[52:53], 0, s[16:17]
	s_lshl_b64 s[16:17], 24, s19
	v_lshl_add_u64 v[36:37], v[52:53], 0, s[0:1]
	v_lshl_add_u64 v[44:45], v[52:53], 0, s[16:17]
	s_lshl_b64 s[16:17], 28, s19
	v_lshl_add_u64 v[54:55], v[36:37], 0, s[0:1]
	v_lshl_add_u64 v[48:49], v[52:53], 0, s[16:17]
	s_lshl_b32 s0, s9, 3
	s_lshl_b64 s[16:17], 20, s19
	global_load_dwordx4 v[28:31], v[52:53], off nt
	global_load_dwordx4 v[32:35], v[36:37], off nt
	s_nop 0
	global_load_dwordx4 v[36:39], v[54:55], off nt
	s_nop 0
	global_load_dwordx4 v[40:43], v[40:41], off nt
	v_lshl_add_u64 v[54:55], v[54:55], 0, s[0:1]
	v_lshl_add_u64 v[56:57], v[52:53], 0, s[16:17]
	global_load_dwordx4 v[44:47], v[44:45], off nt
	s_nop 0
	global_load_dwordx4 v[48:51], v[48:49], off nt
	s_nop 0
	global_load_dwordx4 v[52:55], v[54:55], off nt
	s_nop 0
	global_load_dwordx4 v[56:59], v[56:57], off nt
	s_lshl_b64 s[4:5], s[4:5], s19
	s_lshl_b64 s[4:5], s[4:5], 11
	s_add_u32 s0, s20, s4
	s_addc_u32 s9, s21, s5
	s_bfe_i64 s[4:5], s[8:9], 0x80000
	s_bfe_i64 s[6:7], s[6:7], 0x80000
	s_lshl_b64 s[4:5], s[4:5], 19
	s_add_u32 s0, s0, s4
	s_addc_u32 s8, s9, s5
	s_lshl_b64 s[4:5], s[6:7], 15
	s_add_u32 s4, s0, s4
	s_addc_u32 s5, s8, s5
	v_mov_b32_e32 v11, v3
	s_add_i32 s3, s3, -1
	s_cmp_eq_u32 s3, 0
	s_waitcnt vmcnt(7)
	ds_write_b128 v16, v[28:31]
	s_waitcnt vmcnt(6)
	ds_write2_b32 v17, v32, v33 offset1:1
	ds_write2_b32 v18, v34, v35 offset1:1
	s_waitcnt vmcnt(3)
	ds_write2_b64 v24, v[44:45], v[46:47] offset1:1
	s_waitcnt vmcnt(2)
	ds_write2_b32 v25, v48, v49 offset1:1
	ds_write2_b32 v26, v50, v51 offset1:1
	ds_write2_b64 v19, v[36:37], v[38:39] offset1:1
	ds_write2_b32 v20, v40, v41 offset1:1
	ds_write2_b32 v21, v42, v43 offset1:1
	s_waitcnt vmcnt(1)
	ds_write_b128 v16, v[52:55] offset:4112
	s_waitcnt vmcnt(0)
	ds_write2_b32 v22, v56, v57 offset1:1
	ds_write2_b32 v23, v58, v59 offset1:1
	s_waitcnt lgkmcnt(0)
	s_barrier
	ds_read_b32 v28, v27 offset:1028
	ds_read_b32 v29, v27 offset:3084
	ds_read_b32 v30, v27 offset:5140
	ds_read_b32 v31, v27 offset:7196
	ds_read_b32 v32, v27 offset:6168
	ds_read_b32 v33, v27 offset:4112
	ds_read_b32 v34, v27 offset:2056
	ds_read_b32 v35, v27
	s_waitcnt lgkmcnt(0)
	v_cvt_pk_bf16_f32 v28, v35, v28
	v_cvt_pk_bf16_f32 v29, v34, v29
	v_cvt_pk_bf16_f32 v30, v33, v30
	v_cvt_pk_bf16_f32 v31, v32, v31
	ds_read_b32 v36, v27 offset:1060
	ds_read_b32 v37, v27 offset:3116
	ds_read_b32 v38, v27 offset:5172
	ds_read_b32 v39, v27 offset:7228
	ds_read_b32 v40, v27 offset:6200
	ds_read_b32 v41, v27 offset:4144
	ds_read_b32 v42, v27 offset:2088
	ds_read_b32 v43, v27 offset:32
	v_lshl_add_u64 v[32:33], s[4:5], 0, v[2:3]
	v_lshl_add_u64 v[34:35], v[32:33], 0, v[10:11]
	global_store_dwordx4 v[34:35], v[28:31], off
	v_lshl_add_u64 v[34:35], v[4:5], 1, v[32:33]
	s_cselect_b64 s[4:5], -1, 0
	s_waitcnt lgkmcnt(0)
	v_cvt_pk_bf16_f32 v28, v43, v36
	v_cvt_pk_bf16_f32 v29, v42, v37
	v_cvt_pk_bf16_f32 v30, v41, v38
	v_cvt_pk_bf16_f32 v31, v40, v39
	ds_read_b32 v11, v27 offset:1092
	ds_read_b32 v36, v27 offset:3148
	ds_read_b32 v37, v27 offset:6232
	ds_read_b32 v38, v27 offset:4176
	ds_read_b32 v39, v27 offset:2120
	ds_read_b32 v40, v27 offset:64
	ds_read_b32 v41, v27 offset:5204
	ds_read_b32 v42, v27 offset:7260
	global_store_dwordx4 v[34:35], v[28:31], off
	v_lshl_add_u64 v[34:35], v[6:7], 1, v[32:33]
	v_lshl_add_u64 v[32:33], v[8:9], 1, v[32:33]
	s_waitcnt lgkmcnt(2)
	v_cvt_pk_bf16_f32 v28, v40, v11
	v_cvt_pk_bf16_f32 v29, v39, v36
	s_waitcnt lgkmcnt(1)
	v_cvt_pk_bf16_f32 v30, v38, v41
	s_waitcnt lgkmcnt(0)
	v_cvt_pk_bf16_f32 v31, v37, v42
	ds_read_b32 v11, v27 offset:1124
	ds_read_b32 v36, v27 offset:3180
	ds_read_b32 v37, v27 offset:6264
	ds_read_b32 v38, v27 offset:4208
	ds_read_b32 v39, v27 offset:2152
	ds_read_b32 v40, v27 offset:96
	ds_read_b32 v41, v27 offset:5236
	ds_read_b32 v42, v27 offset:7292
	global_store_dwordx4 v[34:35], v[28:31], off
	s_waitcnt lgkmcnt(2)
	s_nop 0
	v_cvt_pk_bf16_f32 v28, v40, v11
	v_cvt_pk_bf16_f32 v29, v39, v36
	s_waitcnt lgkmcnt(1)
	v_cvt_pk_bf16_f32 v30, v38, v41
	s_waitcnt lgkmcnt(0)
	v_cvt_pk_bf16_f32 v31, v37, v42
	global_store_dwordx4 v[32:33], v[28:31], off
	s_branch .LBB0_1611

; #define SEAM(k) do { if (IN(k) && IN((k) + 1)) xcd_barrier(bar); \
;         if (PROBE_MASK) { const unsigned long long t_ = __builtin_amdgcn_s_memrealtime(); if ((PROBE_MASK >> (k)) & 1u) pr_acc += t_ - pr_t0; pr_t0 = t_; } } while (0)
; __device__ __forceinline__ void convert_deferred(const Ptrs& P, unsigned char* lds, int quota) {
;     const int tid = threadIdx.x, wid = tid >> 6, lane = tid & 63;
;     float* tile = (float*)lds;
;     volatile __attribute__((address_space(3))) int* slot = (volatile __attribute__((address_space(3))) int*)((__attribute__((address_space(3))) unsigned char*)lds + 131072 + 320 + 11000);
;     unsigned* q = (unsigned*)(P.ws + WS_CTL) + CW_DEFQ;
;     for (int n = 0; n < quota; ++n) {
;         __syncthreads();
;         if (tid == 0) *slot = (int)atomicAdd(q, 1u);
;         __syncthreads();
;         const int t = *slot;
;         if (t >= DEF_GU + DEF_DN) break;
;         const bool gu = t < DEF_GU;
;         const float* src = gu ? P.in[34] : P.in[36]; bf16* dst = (bf16*)(P.ws + (gu ? WS_WGU : WS_WDN));
;         const int N = gu ? 2048 : 1024, ntn = N / 256, it = gu ? 2 * NE * 16 * 8 - DEF_GU + t : 2 * NE * 16 * 4 - DEF_DN + (t - DEF_GU);
; __global__ void __launch_bounds__(NT, 2) mega(Args args) {
;     ...
;         g8::gemm_phase<g8::EpiDiffIn, g8::DenseOrder, false, true>(LDSP, D, D, S, E);
;         if (IDLE_LAST(68 * 12)) convert_deferred(P, lds, 4); } SEAM(11);
.LBB0_1851:
	s_abs_i32 s0, s62
	v_cvt_f32_u32_e32 v2, s0
	s_sub_i32 s3, 0, s0
	v_readlane_b32 s56, v254, 40
	s_mov_b32 s1, 0
	v_rcp_iflag_f32_e32 v2, v2
	v_readlane_b32 s57, v254, 41
	v_mul_f32_e32 v2, 0x4f7ffffe, v2
	v_cvt_u32_f32_e32 v2, v2
	s_nop 0
	v_readfirstlane_b32 s4, v2
	s_mul_i32 s3, s3, s4
	s_mul_hi_u32 s3, s4, s3
	s_add_i32 s4, s4, s3
	s_mul_hi_u32 s3, s4, 0x330
	s_mul_i32 s3, s3, s0
	s_sub_i32 s3, 0x330, s3
	s_sub_i32 s4, s3, s0
	s_cmp_ge_u32 s3, s0
	s_cselect_b32 s3, s4, s3
	s_sub_i32 s4, s3, s0
	s_cmp_ge_u32 s3, s0
	s_cselect_b32 s0, s4, s3
	s_cmp_eq_u32 s0, 0
	s_cselect_b64 s[4:5], -1, 0
	s_cmp_lt_i32 s2, s0
	s_cselect_b64 s[6:7], -1, 0
	s_or_b64 s[4:5], s[4:5], s[6:7]
	s_and_b64 vcc, exec, s[4:5]
	s_cbranch_vccnz .LBB0_1861
	v_and_b32_e32 v2, 0x7c, v218
	v_lshlrev_b32_e32 v3, 5, v0
	s_movk_i32 s0, 0x400
	v_and_or_b32 v12, v3, s0, v2
	v_bfe_u32 v2, v0, 3, 3
	v_lshl_or_b32 v4, v1, 5, v2
	v_lshlrev_b32_e32 v2, 3, v0
	v_lshl_add_u32 v11, v182, 4, 0
	v_and_b32_e32 v2, 56, v2
	v_mul_u32_u24_e32 v16, 0x2020, v1
	v_mov_b32_e32 v3, 0
	s_waitcnt vmcnt(0)
	v_lshl_add_u32 v27, v4, 2, 0
	v_mul_u32_u24_e32 v28, 0x404, v2
	v_lshlrev_b32_e32 v10, 6, v4
	s_add_i32 s10, 0, 0x22c38
	v_add_u32_e32 v16, v11, v16
	v_and_b32_e32 v13, 0xfc, v218
	v_and_b32_e32 v14, 56, v179
	s_mov_b32 s3, 4
	v_or_b32_e32 v4, 0x200, v10
	v_mov_b32_e32 v5, v3
	v_or_b32_e32 v6, 0x400, v10
	v_mov_b32_e32 v7, v3
	v_or_b32_e32 v8, 0x600, v10
	v_mov_b32_e32 v9, v3
	v_mov_b32_e32 v15, s10
	s_movk_i32 s11, 0x833
	s_movk_i32 s12, 0x800
	s_mov_b32 s13, 0x1104e000
	s_movk_i32 s14, 0x7cc
	v_add_u32_e32 v17, 0x404, v16
	v_add_u32_e32 v18, 0x40c, v16
	v_add_u32_e32 v19, 0x808, v16
	v_add_u32_e32 v20, 0xc0c, v16
	v_add_u32_e32 v21, 0xc14, v16
	v_add_u32_e32 v22, 0x1414, v16
	v_add_u32_e32 v23, 0x141c, v16
	v_add_u32_e32 v24, 0x1818, v16
	v_add_u32_e32 v25, 0x1c1c, v16
	v_add_u32_e32 v26, 0x1c24, v16
	v_lshlrev_b32_e32 v2, 1, v2
	v_add_u32_e32 v27, v27, v28
	v_lshlrev_b32_e32 v10, 1, v10
	s_branch .LBB0_1854

; __device__ __forceinline__ unsigned g8_cvt_pk(float lo, float hi) { unsigned r; asm volatile("v_cvt_pk_bf16_f32 %0, %1, %2" : "=v"(r) : "v"(lo), "v"(hi)); return r; }
; __device__ __forceinline__ void convert_deferred(const Ptrs& P, unsigned char* lds, int quota) {
;     ...
;     for (int n = 0; n < quota; ++n) {
;         __syncthreads();
;         if (tid == 0) *slot = (int)atomicAdd(q, 1u);
;         __syncthreads();
;         const int t = *slot;
;         if (t >= DEF_GU + DEF_DN) break;
;         const bool gu = t < DEF_GU;
;         const float* src = gu ? P.in[34] : P.in[36]; bf16* dst = (bf16*)(P.ws + (gu ? WS_WGU : WS_WDN));
;         const int N = gu ? 2048 : 1024, ntn = N / 256, it = gu ? 2 * NE * 16 * 8 - DEF_GU + t : 2 * NE * 16 * 4 - DEF_DN + (t - DEF_GU);
;         f32x4 cur[8];
;         bt_load(src, N, gu ? 1 : 0, it, ntn, cur);
; #pragma unroll
;         for (int i = 0; i < 8; ++i) { float* tp = tile + (wid * 8 + i) * 257 + lane * 4; tp[0] = cur[i][0]; tp[1] = cur[i][1]; tp[2] = cur[i][2]; tp[3] = cur[i][3]; }
;         __syncthreads();
;         const int per = 16 * ntn, z = it / per, r = it % per, kt = r / ntn, nt = r % ntn;
;         bf16* d = dst + (size_t)z * N * 1024 + (((size_t)nt * 16 + kt) << 14);
;         const int kc = lane & 7;
; #pragma unroll
;         for (int pss = 0; pss < 4; ++pss) {
;             const int nn = wid * 32 + pss * 8 + (lane >> 3); float f[8];
; #pragma unroll
;             for (int j = 0; j < 8; ++j) f[j] = tile[(kc * 8 + j) * 257 + nn];
;             u32x4 w; w.x = g8_cvt_pk(f[0], f[1]); w.y = g8_cvt_pk(f[2], f[3]); w.z = g8_cvt_pk(f[4], f[5]); w.w = g8_cvt_pk(f[6], f[7]);
;             *(u32x4*)(d + nn * 64 + kc * 8) = w;
;         }
.LBB0_1858:
	s_or_b64 exec, exec, s[4:5]
	s_waitcnt lgkmcnt(0)
	s_barrier
	ds_read_b32 v11, v15
	s_mov_b64 s[4:5], -1
	s_waitcnt lgkmcnt(0)
	v_cmp_lt_i32_e32 vcc, s11, v11
	v_readfirstlane_b32 s0, v11
	s_cbranch_vccnz .LBB0_1853
	s_cmpk_gt_i32 s0, 0x577
	s_cselect_b64 vcc, -1, 0
	s_and_b64 s[4:5], vcc, exec
	s_cselect_b32 s4, s13, 0x104e000
	s_cselect_b32 s9, 0x400, s12
	s_cselect_b32 s15, s73, s69
	s_cselect_b32 s20, s72, s68
	s_cselect_b32 s5, s14, 0x1a88
	s_cselect_b32 s16, 20, 21
	s_cselect_b32 s21, 10, 11
	s_add_u32 s22, s78, s4
	s_addc_u32 s23, s79, 0
	s_lshr_b32 s6, s9, 4
	s_abs_i32 s4, s6
	v_cvt_f32_u32_e32 v11, s4
	s_sub_i32 s17, 0, s4
	s_add_i32 s5, s5, s0
	s_abs_i32 s7, s5
	v_rcp_iflag_f32_e32 v11, v11
	s_xor_b32 s0, s5, s6
	s_lshr_b32 s8, s9, 8
	s_ashr_i32 s0, s0, 31
	v_mul_f32_e32 v11, 0x4f7ffffe, v11
	v_cvt_u32_f32_e32 v11, v11
	s_nop 0
	v_readfirstlane_b32 s24, v11
	s_mul_i32 s17, s17, s24
	s_mul_hi_u32 s17, s24, s17
	s_add_i32 s24, s24, s17
	s_mul_hi_u32 s17, s7, s24
	s_mul_i32 s24, s17, s4
	s_sub_i32 s7, s7, s24
	s_add_i32 s24, s17, 1
	s_sub_i32 s25, s7, s4
	s_cmp_ge_u32 s7, s4
	s_cselect_b32 s17, s24, s17
	s_cselect_b32 s7, s25, s7
	s_add_i32 s24, s17, 1
	s_cmp_ge_u32 s7, s4
	s_cselect_b32 s4, s24, s17
	s_xor_b32 s4, s4, s0
	s_sub_i32 s4, s4, s0
	s_sext_i32_i8 s0, s8
	v_cvt_f32_i32_e32 v11, s0
	s_mul_i32 s6, s4, s6
	s_sub_i32 s5, s5, s6
	v_cvt_f32_i32_e32 v28, s5
	v_rcp_iflag_f32_e32 v29, v11
	s_xor_b32 s0, s5, s0
	s_ashr_i32 s0, s0, 30
	s_or_b32 s0, s0, 1
	v_mul_f32_e32 v29, v28, v29
	v_trunc_f32_e32 v29, v29
	v_fma_f32 v28, -v29, v11, v28
	v_cvt_i32_f32_e32 v29, v29
	v_cmp_ge_f32_e64 s[6:7], |v28|, |v11|
	s_and_b64 s[6:7], s[6:7], exec
	s_cselect_b32 s0, s0, 0
	v_readfirstlane_b32 s6, v29
	s_add_i32 s6, s6, s0
	s_mul_i32 s7, s6, s8
	s_sub_i32 s8, s5, s7
	s_sext_i32_i8 s5, s8
	v_lshl_add_u32 v11, s5, 7, v12
	v_lshl_or_b32 v28, s5, 8, v13
	s_ashr_i32 s5, s4, 31
	s_sext_i32_i8 s0, s6
	s_lshl_b64 s[16:17], s[4:5], s16
	v_lshl_or_b32 v30, s0, 6, v14
	s_lshl_b64 s[16:17], s[16:17], 2
	v_ashrrev_i32_e32 v31, 31, v30
	s_add_u32 s16, s20, s16
	v_cndmask_b32_e32 v28, v11, v28, vcc
	s_addc_u32 s17, s15, s17
	v_lshlrev_b64 v[30:31], s21, v[30:31]
	v_lshl_add_u64 v[30:31], v[30:31], 2, s[16:17]
	v_ashrrev_i32_e32 v29, 31, v28
	v_lshl_add_u64 v[52:53], v[28:29], 2, v[30:31]
	s_lshl_b64 s[16:17], 12, s21
	s_lshl_b32 s0, s9, 2
	v_lshl_add_u64 v[40:41], v[52:53], 0, s[16:17]
	s_lshl_b64 s[16:17], 24, s21
	v_lshl_add_u64 v[36:37], v[52:53], 0, s[0:1]
	v_lshl_add_u64 v[44:45], v[52:53], 0, s[16:17]
	s_lshl_b64 s[16:17], 28, s21
	v_lshl_add_u64 v[54:55], v[36:37], 0, s[0:1]
	v_lshl_add_u64 v[48:49], v[52:53], 0, s[16:17]
	s_lshl_b32 s0, s9, 3
	s_lshl_b64 s[16:17], 20, s21
	global_load_dwordx4 v[28:31], v[52:53], off nt
	global_load_dwordx4 v[32:35], v[36:37], off nt
	s_nop 0
	global_load_dwordx4 v[36:39], v[54:55], off nt
	s_nop 0
	global_load_dwordx4 v[40:43], v[40:41], off nt
	v_lshl_add_u64 v[54:55], v[54:55], 0, s[0:1]
	v_lshl_add_u64 v[56:57], v[52:53], 0, s[16:17]
	global_load_dwordx4 v[44:47], v[44:45], off nt
	s_nop 0
	global_load_dwordx4 v[48:51], v[48:49], off nt
	s_nop 0
	global_load_dwordx4 v[52:55], v[54:55], off nt
	s_nop 0
	global_load_dwordx4 v[56:59], v[56:57], off nt
	s_lshl_b64 s[4:5], s[4:5], s21
	s_lshl_b64 s[4:5], s[4:5], 11
	s_add_u32 s0, s22, s4
	s_addc_u32 s9, s23, s5
	s_bfe_i64 s[4:5], s[8:9], 0x80000
	s_bfe_i64 s[6:7], s[6:7], 0x80000
	s_lshl_b64 s[4:5], s[4:5], 19
	s_add_u32 s0, s0, s4
	s_addc_u32 s8, s9, s5
	s_lshl_b64 s[4:5], s[6:7], 15
	s_add_u32 s4, s0, s4
	s_addc_u32 s5, s8, s5
	v_mov_b32_e32 v11, v3
	s_add_i32 s3, s3, -1
	s_cmp_eq_u32 s3, 0
	s_waitcnt vmcnt(7)
	ds_write_b128 v16, v[28:31]
	s_waitcnt vmcnt(6)
	ds_write2_b32 v17, v32, v33 offset1:1
	ds_write2_b32 v18, v34, v35 offset1:1
	s_waitcnt vmcnt(3)
	ds_write2_b64 v24, v[44:45], v[46:47] offset1:1
	s_waitcnt vmcnt(2)
	ds_write2_b32 v25, v48, v49 offset1:1
	ds_write2_b32 v26, v50, v51 offset1:1
	ds_write2_b64 v19, v[36:37], v[38:39] offset1:1
	ds_write2_b32 v20, v40, v41 offset1:1
	ds_write2_b32 v21, v42, v43 offset1:1
	s_waitcnt vmcnt(1)
	ds_write_b128 v16, v[52:55] offset:4112
	s_waitcnt vmcnt(0)
	ds_write2_b32 v22, v56, v57 offset1:1
	ds_write2_b32 v23, v58, v59 offset1:1
	s_waitcnt lgkmcnt(0)
	s_barrier
	ds_read_b32 v28, v27 offset:1028
	ds_read_b32 v29, v27 offset:3084
	ds_read_b32 v30, v27 offset:5140
	ds_read_b32 v31, v27 offset:7196
	ds_read_b32 v32, v27 offset:6168
	ds_read_b32 v33, v27 offset:4112
	ds_read_b32 v34, v27 offset:2056
	ds_read_b32 v35, v27
	s_waitcnt lgkmcnt(0)
	v_cvt_pk_bf16_f32 v28, v35, v28
	v_cvt_pk_bf16_f32 v29, v34, v29
	v_cvt_pk_bf16_f32 v30, v33, v30
	v_cvt_pk_bf16_f32 v31, v32, v31
	ds_read_b32 v36, v27 offset:1060
	ds_read_b32 v37, v27 offset:3116
	ds_read_b32 v38, v27 offset:5172
	ds_read_b32 v39, v27 offset:7228
	ds_read_b32 v40, v27 offset:6200
	ds_read_b32 v41, v27 offset:4144
	ds_read_b32 v42, v27 offset:2088
	ds_read_b32 v43, v27 offset:32
	v_lshl_add_u64 v[32:33], s[4:5], 0, v[2:3]
	v_lshl_add_u64 v[34:35], v[32:33], 0, v[10:11]
	global_store_dwordx4 v[34:35], v[28:31], off
	v_lshl_add_u64 v[34:35], v[4:5], 1, v[32:33]
	s_cselect_b64 s[4:5], -1, 0
	s_waitcnt lgkmcnt(0)
	v_cvt_pk_bf16_f32 v28, v43, v36
	v_cvt_pk_bf16_f32 v29, v42, v37
	v_cvt_pk_bf16_f32 v30, v41, v38
	v_cvt_pk_bf16_f32 v31, v40, v39
	ds_read_b32 v11, v27 offset:1092
	ds_read_b32 v36, v27 offset:3148
	ds_read_b32 v37, v27 offset:6232
	ds_read_b32 v38, v27 offset:4176
	ds_read_b32 v39, v27 offset:2120
	ds_read_b32 v40, v27 offset:64
	ds_read_b32 v41, v27 offset:5204
	ds_read_b32 v42, v27 offset:7260
	global_store_dwordx4 v[34:35], v[28:31], off
	v_lshl_add_u64 v[34:35], v[6:7], 1, v[32:33]
	v_lshl_add_u64 v[32:33], v[8:9], 1, v[32:33]
	s_waitcnt lgkmcnt(2)
	v_cvt_pk_bf16_f32 v28, v40, v11
	v_cvt_pk_bf16_f32 v29, v39, v36
	s_waitcnt lgkmcnt(1)
	v_cvt_pk_bf16_f32 v30, v38, v41
	s_waitcnt lgkmcnt(0)
	v_cvt_pk_bf16_f32 v31, v37, v42
	ds_read_b32 v11, v27 offset:1124
	ds_read_b32 v36, v27 offset:3180
	ds_read_b32 v37, v27 offset:6264
	ds_read_b32 v38, v27 offset:4208
	ds_read_b32 v39, v27 offset:2152
	ds_read_b32 v40, v27 offset:96
	ds_read_b32 v41, v27 offset:5236
	ds_read_b32 v42, v27 offset:7292
	global_store_dwordx4 v[34:35], v[28:31], off
	s_waitcnt lgkmcnt(2)
	s_nop 0
	v_cvt_pk_bf16_f32 v28, v40, v11
	v_cvt_pk_bf16_f32 v29, v39, v36
	s_waitcnt lgkmcnt(1)
	v_cvt_pk_bf16_f32 v30, v38, v41
	s_waitcnt lgkmcnt(0)
	v_cvt_pk_bf16_f32 v31, v37, v42
	global_store_dwordx4 v[32:33], v[28:31], off
	s_branch .LBB0_1853

; #define PSUB_AT(k) do { if (PROBE_SUB == (k) && DK == PROBE_SUBDK) sacc = __builtin_amdgcn_readfirstlane(sacc + ((unsigned)__builtin_readcyclecounter() - ps_t0_)); } while (0)
; #define SBAR() __builtin_amdgcn_sched_barrier(0)
; #define SLOAD(k0) do { const unsigned so_k = (unsigned)((k0) * ldk) * 2u, so_v = (unsigned)((k0) * ldv) * 2u; \
;         _Pragma("unroll") for (int i = 0; i < KP; ++i) ks[i] = __builtin_amdgcn_raw_buffer_load_b128(krs, kgo[i], so_k, 0); \
;         vs0 = __builtin_amdgcn_raw_buffer_load_b128(vrs, vgo, so_v, 0); vs1 = __builtin_amdgcn_raw_buffer_load_b128(vrs, vgo + vstep, so_v, 0); } while (0)
; template <int DK, bool PF, bool EARLY, bool PFD = false> ...
;     ...
;         const char* Kb = K_lds + cur * SHM_K;
; #pragma unroll
;         for (int d0 = 0; d0 < NQ; ++d0) {
;             const bf16x8 b0 = *reinterpret_cast<const bf16x8*>(Kb + kra_(d0 & 3) + (d0 >> 2) * 128);
;             const bf16x8 b1 = *reinterpret_cast<const bf16x8*>(Kb + kra_(d0 & 3) + (d0 >> 2) * 128 + 32 * DK * 2);
;             p0 = __builtin_amdgcn_mfma_f32_32x32x16_bf16(b0, qr[d0], p0, 0, 0, 0);
;             p1 = __builtin_amdgcn_mfma_f32_32x32x16_bf16(b1, qr[d0], p1, 0, 0, 0);
;             if ((d0 & 3) == 3) SBAR();
;         }
;         PSUB_AT(1);
;         if (!EARLY && j + 1 < ntile) SLOAD((j + 1) * 64);
;         float ps = 0.f, ps1 = 0.f;
; #pragma unroll
;         for (int r = 0; r < 16; ++r) { p0[r] = __builtin_amdgcn_exp2f(p0[r]); p1[r] = __builtin_amdgcn_exp2f(p1[r]); ps += p0[r]; asm("" : "+v"(ps)); ps1 += p1[r]; asm("" : "+v"(ps1)); }
;         l_reg += ps + ps1;
;         bf16x8 pa0, pa1, pa2, pa3;
;     ...
;         PK4(p0, 0, pa0); PK4(p0, 8, pa1); PK4(p1, 0, pa2); PK4(p1, 8, pa3);
;     ...
;         PSUB_AT(2);
;         const int vb = vb0 + cur * SHM_V;
;         pv_one<0>(o[0], vb, pa0, pa1, pa2, pa3); pv_one<1>(o[1], vb, pa0, pa1, pa2, pa3); pv_one<2>(o[2], vb, pa0, pa1, pa2, pa3); pv_one<3>(o[3], vb, pa0, pa1, pa2, pa3);
.LBB0_1932:
	s_and_b32 s13, s50, 1
	s_lshl_b32 s12, s13, 13
	v_add_u32_e32 v138, s12, v198
	v_add_u32_e32 v86, v138, v187
	v_add_u32_e32 v134, v138, v200
	v_add_u32_e32 v135, v138, v201
	v_add_u32_e32 v136, v138, v202
	ds_read_b128 v[226:229], v86
	ds_read_b128 v[230:233], v86 offset:4096
	ds_read_b128 v[234:237], v134
	ds_read_b128 v[238:241], v134 offset:4096
	ds_read_b128 v[242:245], v135
	ds_read_b128 v[246:249], v135 offset:4096
	ds_read_b128 v[250:253], v136
	ds_read_b128 v[218:221], v136 offset:4096
	s_add_i32 s33, s51, 0xfff40000
	buffer_load_dwordx4 v[130:133], v145, s[16:19], s33 offen
	buffer_load_dwordx4 v[134:137], v186, s[20:23], s33 offen
	buffer_load_dwordx4 v[138:141], v195, s[20:23], s33 offen
	s_waitcnt lgkmcnt(7)
	v_mfma_f32_32x32x16_bf16 v[98:113], v[226:229], v[126:129], v[2:17]
	s_waitcnt lgkmcnt(6)
	v_mfma_f32_32x32x16_bf16 v[82:97], v[230:233], v[126:129], v[2:17]
	s_waitcnt lgkmcnt(5)
	v_mfma_f32_32x32x16_bf16 v[98:113], v[234:237], v[122:125], v[98:113]
	s_waitcnt lgkmcnt(4)
	v_mfma_f32_32x32x16_bf16 v[82:97], v[238:241], v[122:125], v[82:97]
	s_waitcnt lgkmcnt(3)
	v_mfma_f32_32x32x16_bf16 v[98:113], v[242:245], v[118:121], v[98:113]
	s_waitcnt lgkmcnt(2)
	v_mfma_f32_32x32x16_bf16 v[82:97], v[246:249], v[118:121], v[82:97]
	s_waitcnt lgkmcnt(1)
	v_mfma_f32_32x32x16_bf16 v[98:113], v[250:253], v[114:117], v[98:113]
	s_waitcnt lgkmcnt(0)
	v_mfma_f32_32x32x16_bf16 v[82:97], v[218:221], v[114:117], v[82:97]
	s_lshl_b32 s13, s13, 14
	v_add_u32_e32 v253, s13, v199
	ds_read_b64_tr_b16 v[226:227], v253 offset:0x0
	ds_read_b64_tr_b16 v[228:229], v253 offset:0x800
	ds_read_b64_tr_b16 v[230:231], v253 offset:0x1000
	ds_read_b64_tr_b16 v[232:233], v253 offset:0x1800
	ds_read_b64_tr_b16 v[234:235], v253 offset:0x2000
	ds_read_b64_tr_b16 v[236:237], v253 offset:0x2800
	ds_read_b64_tr_b16 v[238:239], v253 offset:0x3000
	ds_read_b64_tr_b16 v[240:241], v253 offset:0x3800
	s_nop 8
	v_exp_f32_e32 v98, v98
	s_nop 1
	v_exp_f32_e32 v159, v82
	v_exp_f32_e32 v99, v99
	v_exp_f32_e32 v163, v83
	v_add_f32_e32 v82, 0, v98
	v_add_f32_e32 v161, 0, v159
	v_exp_f32_e32 v100, v100
	v_exp_f32_e32 v101, v101
	v_add_f32_e32 v82, v99, v82
	v_add_f32_e32 v83, v163, v161
	v_exp_f32_e32 v161, v84
	v_exp_f32_e32 v165, v85
	v_add_f32_e32 v82, v100, v82
	v_exp_f32_e32 v102, v102
	v_exp_f32_e32 v167, v86
	v_add_f32_e32 v83, v161, v83
	v_add_f32_e32 v82, v101, v82
	v_exp_f32_e32 v86, v103
	v_exp_f32_e32 v103, v87
	v_add_f32_e32 v83, v165, v83
	v_add_f32_e32 v82, v102, v82
	v_exp_f32_e32 v87, v104
	v_exp_f32_e32 v104, v88
	v_add_f32_e32 v83, v167, v83
	v_add_f32_e32 v82, v86, v82
	v_exp_f32_e32 v88, v105
	v_exp_f32_e32 v105, v89
	v_add_f32_e32 v83, v103, v83
	v_add_f32_e32 v82, v87, v82
	v_exp_f32_e32 v89, v106
	v_exp_f32_e32 v106, v90
	v_add_f32_e32 v83, v104, v83
	v_add_f32_e32 v82, v88, v82
	v_exp_f32_e32 v90, v107
	v_exp_f32_e32 v107, v91
	v_add_f32_e32 v83, v105, v83
	v_add_f32_e32 v82, v89, v82
	v_exp_f32_e32 v91, v108
	v_exp_f32_e32 v108, v92
	v_add_f32_e32 v83, v106, v83
	v_add_f32_e32 v82, v90, v82
	v_exp_f32_e32 v92, v109
	v_exp_f32_e32 v109, v93
	v_add_f32_e32 v83, v107, v83
	v_add_f32_e32 v82, v91, v82
	v_exp_f32_e32 v93, v110
	v_exp_f32_e32 v110, v94
	v_add_f32_e32 v83, v108, v83
	v_add_f32_e32 v82, v92, v82
	v_exp_f32_e32 v94, v111
	v_exp_f32_e32 v111, v95
	v_add_f32_e32 v83, v109, v83
	v_add_f32_e32 v82, v93, v82
	v_exp_f32_e32 v95, v112
	v_exp_f32_e32 v112, v96
	v_add_f32_e32 v83, v110, v83
	v_add_f32_e32 v82, v94, v82
	v_exp_f32_e32 v96, v113
	v_add_f32_e32 v83, v111, v83
	v_add_f32_e32 v82, v95, v82
	v_exp_f32_e32 v113, v97
	v_add_f32_e32 v83, v112, v83
	v_add_f32_e32 v82, v96, v82
	v_cvt_pk_bf16_f32 v84, v98, v99
	v_cvt_pk_bf16_f32 v85, v100, v101
	v_cvt_pk_bf16_f32 v86, v102, v86
	v_cvt_pk_bf16_f32 v87, v87, v88
	v_cvt_pk_bf16_f32 v88, v89, v90
	v_cvt_pk_bf16_f32 v89, v91, v92
	v_cvt_pk_bf16_f32 v90, v93, v94
	v_cvt_pk_bf16_f32 v91, v95, v96
	v_cvt_pk_bf16_f32 v92, v159, v163
	v_cvt_pk_bf16_f32 v93, v161, v165
	v_cvt_pk_bf16_f32 v94, v167, v103
	v_cvt_pk_bf16_f32 v95, v104, v105
	v_cvt_pk_bf16_f32 v96, v106, v107
	v_cvt_pk_bf16_f32 v97, v108, v109
	v_cvt_pk_bf16_f32 v98, v110, v111
	v_cvt_pk_bf16_f32 v99, v112, v113
	v_add_u32_e32 v112, s13, v199
	v_add_f32_e32 v83, v113, v83
	v_permlane32_swap_b32_e32 v84, v86
	v_permlane32_swap_b32_e32 v85, v87
	v_permlane32_swap_b32_e32 v88, v90
	v_permlane32_swap_b32_e32 v89, v91
	v_permlane32_swap_b32_e32 v92, v94
	v_permlane32_swap_b32_e32 v93, v95
	v_permlane32_swap_b32_e32 v96, v98
	v_permlane32_swap_b32_e32 v97, v99
	s_waitcnt lgkmcnt(0)
; #define PSUB_AT(k) do { if (PROBE_SUB == (k) && DK == PROBE_SUBDK) sacc = __builtin_amdgcn_readfirstlane(sacc + ((unsigned)__builtin_readcyclecounter() - ps_t0_)); } while (0)
; #define SBAR() __builtin_amdgcn_sched_barrier(0)
; template <int OFF> __device__ __forceinline__ s16x4 tr_read(int vb) { s16x4 r; asm volatile("ds_read_b64_tr_b16 %0, %1 offset:%2" : "=&v"(r) : "v"(vb), "i"(OFF) : "memory"); return r; }
; #define SWRITE(b) do { _Pragma("unroll") for (int i = 0; i < KP; ++i) *reinterpret_cast<u32x4*>(K_lds + (b) * SHM_K + kst[i]) = ks[i]; \
;         *reinterpret_cast<u32x4*>(V_lds + (b) * SHM_V + vst0) = vs0; *reinterpret_cast<u32x4*>(V_lds + (b) * SHM_V + vst0 + vst1d) = vs1; } while (0)
; template <int D0> __device__ __forceinline__ void pv_one(f32x16& od, int vb, bf16x8 pa0, bf16x8 pa1, bf16x8 pa2, bf16x8 pa3) {
;     const s16x4 l0 = tr_read<v_rd_off(D0, 0, 0)>(vb), h0 = tr_read<v_rd_off(D0, 0, 1)>(vb), l1 = tr_read<v_rd_off(D0, 1, 0)>(vb), h1 = tr_read<v_rd_off(D0, 1, 1)>(vb);
;     const s16x4 l2 = tr_read<v_rd_off(D0, 2, 0)>(vb), h2 = tr_read<v_rd_off(D0, 2, 1)>(vb), l3 = tr_read<v_rd_off(D0, 3, 0)>(vb), h3 = tr_read<v_rd_off(D0, 3, 1)>(vb);
;     asm volatile("s_waitcnt lgkmcnt(0)" ::: "memory"); SBAR();
;     ...
;     od = __builtin_amdgcn_mfma_f32_32x32x16_bf16(pa0, PK(l0, h0), od, 0, 0, 0);
;     od = __builtin_amdgcn_mfma_f32_32x32x16_bf16(pa1, PK(l1, h1), od, 0, 0, 0);
;     od = __builtin_amdgcn_mfma_f32_32x32x16_bf16(pa2, PK(l2, h2), od, 0, 0, 0);
;     od = __builtin_amdgcn_mfma_f32_32x32x16_bf16(pa3, PK(l3, h3), od, 0, 0, 0);
; template <int DK, bool PF, bool EARLY, bool PFD = false> ...
;     ...
;         const int vb = vb0 + cur * SHM_V;
;         pv_one<0>(o[0], vb, pa0, pa1, pa2, pa3); pv_one<1>(o[1], vb, pa0, pa1, pa2, pa3); pv_one<2>(o[2], vb, pa0, pa1, pa2, pa3); pv_one<3>(o[3], vb, pa0, pa1, pa2, pa3);
;         PSUB_AT(3);
;         if (j + 1 < ntile) SWRITE(cur ^ 1);
;         if (j + 3 < ntile) PREFETCH(j + 3);
;         __syncthreads();
	v_mfma_f32_32x32x16_bf16 v[66:81], v[84:87], v[226:229], v[66:81]
	ds_read_b64_tr_b16 v[100:101], v112 offset:0x200
	ds_read_b64_tr_b16 v[102:103], v112 offset:0xa00
	v_mfma_f32_32x32x16_bf16 v[66:81], v[88:91], v[230:233], v[66:81]
	ds_read_b64_tr_b16 v[104:105], v112 offset:0x1200
	ds_read_b64_tr_b16 v[106:107], v112 offset:0x1a00
	v_mfma_f32_32x32x16_bf16 v[66:81], v[92:95], v[234:237], v[66:81]
	ds_read_b64_tr_b16 v[108:109], v112 offset:0x2200
	ds_read_b64_tr_b16 v[110:111], v112 offset:0x2a00
	ds_read_b64_tr_b16 v[222:223], v112 offset:0x3200
	ds_read_b64_tr_b16 v[224:225], v112 offset:0x3a00
	v_mfma_f32_32x32x16_bf16 v[66:81], v[96:99], v[238:241], v[66:81]
	s_waitcnt lgkmcnt(6)
	v_mfma_f32_32x32x16_bf16 v[50:65], v[84:87], v[100:103], v[50:65]
	ds_read_b64_tr_b16 v[100:101], v112 offset:0x400
	ds_read_b64_tr_b16 v[102:103], v112 offset:0xc00
	s_waitcnt lgkmcnt(6)
	v_mfma_f32_32x32x16_bf16 v[50:65], v[88:91], v[104:107], v[50:65]
	ds_read_b64_tr_b16 v[104:105], v112 offset:0x1400
	ds_read_b64_tr_b16 v[106:107], v112 offset:0x1c00
	s_waitcnt lgkmcnt(6)
	v_mfma_f32_32x32x16_bf16 v[50:65], v[92:95], v[108:111], v[50:65]
	ds_read_b64_tr_b16 v[108:109], v112 offset:0x2400
	ds_read_b64_tr_b16 v[110:111], v112 offset:0x2c00
	ds_read_b64_tr_b16 v[218:219], v112 offset:0x3400
	ds_read_b64_tr_b16 v[220:221], v112 offset:0x3c00
	s_waitcnt lgkmcnt(8)
	v_mfma_f32_32x32x16_bf16 v[50:65], v[96:99], v[222:225], v[50:65]
	s_waitcnt lgkmcnt(6)
	v_mfma_f32_32x32x16_bf16 v[34:49], v[84:87], v[100:103], v[34:49]
	ds_read_b64_tr_b16 v[100:101], v112 offset:0x600
	ds_read_b64_tr_b16 v[102:103], v112 offset:0xe00
	s_waitcnt lgkmcnt(6)
	v_mfma_f32_32x32x16_bf16 v[34:49], v[88:91], v[104:107], v[34:49]
	ds_read_b64_tr_b16 v[104:105], v112 offset:0x1600
	ds_read_b64_tr_b16 v[106:107], v112 offset:0x1e00
	s_waitcnt lgkmcnt(6)
	v_mfma_f32_32x32x16_bf16 v[34:49], v[92:95], v[108:111], v[34:49]
	ds_read_b64_tr_b16 v[108:109], v112 offset:0x2600
	ds_read_b64_tr_b16 v[110:111], v112 offset:0x2e00
	ds_read_b64_tr_b16 v[222:223], v112 offset:0x3600
	ds_read_b64_tr_b16 v[224:225], v112 offset:0x3e00
	s_waitcnt lgkmcnt(8)
	v_mfma_f32_32x32x16_bf16 v[34:49], v[96:99], v[218:221], v[34:49]
	s_waitcnt lgkmcnt(6)
	v_mfma_f32_32x32x16_bf16 v[18:33], v[84:87], v[100:103], v[18:33]
	s_waitcnt lgkmcnt(0)
	s_xor_b32 s12, s12, 0x2000
	v_add_u32_e32 v84, s12, v196
	s_xor_b32 s12, s13, 0x4000
	s_cmpk_lt_u32 s50, 0x41
	s_waitcnt vmcnt(2)
	ds_write_b128 v84, v[130:133]
	v_add_u32_e32 v84, s12, v197
	s_cselect_b64 s[12:13], -1, 0
	v_mfma_f32_32x32x16_bf16 v[18:33], v[88:91], v[104:107], v[18:33]
	s_and_b64 s[36:37], s[6:7], s[12:13]
	s_waitcnt vmcnt(1)
	ds_write_b128 v84, v[134:137]
	s_waitcnt vmcnt(0)
	ds_write_b128 v84, v[138:141] offset:8192
	v_mfma_f32_32x32x16_bf16 v[18:33], v[92:95], v[108:111], v[18:33]
	v_mfma_f32_32x32x16_bf16 v[18:33], v[96:99], v[222:225], v[18:33]
	s_and_saveexec_b64 s[12:13], s[36:37]
	s_cbranch_execz .LBB0_1931
	s_and_saveexec_b64 s[36:37], s[26:27]
	s_xor_b64 s[36:37], exec, s[36:37]
	s_lshl_b32 s33, s50, 6
	s_addk_i32 s33, 0xc0
	v_add_u32_e32 v84, s33, v189
	v_mul_lo_u32 v84, v84, s42
	v_or_b32_e32 v84, v84, v190
	v_lshl_add_u32 v84, v84, 1, s49
	s_andn2_saveexec_b64 s[36:37], s[36:37]
	s_cbranch_execz .LBB0_1930
	v_add_u32_e32 v84, s51, v206
	s_branch .LBB0_1930

; #define SEAM(k) do { if (IN(k) && IN((k) + 1)) xcd_barrier(bar); \
;         if (PROBE_MASK) { const unsigned long long t_ = __builtin_amdgcn_s_memrealtime(); if ((PROBE_MASK >> (k)) & 1u) pr_acc += t_ - pr_t0; pr_t0 = t_; } } while (0)
; __device__ __forceinline__ void convert_deferred(const Ptrs& P, unsigned char* lds, int quota) {
;     const int tid = threadIdx.x, wid = tid >> 6, lane = tid & 63;
;     float* tile = (float*)lds;
;     volatile __attribute__((address_space(3))) int* slot = (volatile __attribute__((address_space(3))) int*)((__attribute__((address_space(3))) unsigned char*)lds + 131072 + 320 + 11000);
;     unsigned* q = (unsigned*)(P.ws + WS_CTL) + CW_DEFQ;
;     for (int n = 0; n < quota; ++n) {
;         __syncthreads();
;         if (tid == 0) *slot = (int)atomicAdd(q, 1u);
;         __syncthreads();
;         const int t = *slot;
;         if (t >= DEF_GU + DEF_DN) break;
;         const bool gu = t < DEF_GU;
;         const float* src = gu ? P.in[34] : P.in[36]; bf16* dst = (bf16*)(P.ws + (gu ? WS_WGU : WS_WDN));
;         const int N = gu ? 2048 : 1024, ntn = N / 256, it = gu ? 2 * NE * 16 * 8 - DEF_GU + t : 2 * NE * 16 * 4 - DEF_DN + (t - DEF_GU);
; __global__ void __launch_bounds__(NT, 2) mega(Args args) {
;     ...
;         g8::gemm_phase<g8::EpiOut, g8::DenseOrder, false, true>(LDSP, D, D, S, E); } SEAM(14);
;     if (IN(15)) { ph_norm2_router(P, lds, 1, 1); convert_deferred(P, lds, 1 << 20); } SEAM(15);
.LBB0_2278:
	v_and_b32_e32 v2, 0x7c, v179
	v_lshlrev_b32_e32 v3, 5, v0
	s_movk_i32 s0, 0x400
	v_and_or_b32 v12, v3, s0, v2
	v_lshrrev_b32_e32 v2, 3, v0
	v_and_b32_e32 v14, 56, v2
	v_lshrrev_b32_e32 v2, 3, v182
	v_lshl_or_b32 v4, v1, 5, v2
	v_lshl_add_u32 v5, v182, 4, 0
	v_and_b32_e32 v2, 56, v188
	v_lshl_add_u32 v7, v4, 2, 0
	v_mul_u32_u24_e32 v11, 0x2020, v1
	v_lshlrev_b32_e32 v4, 6, v4
	v_mul_u32_u24_e32 v9, 0x404, v2
	v_or_b32_e32 v6, 0x200, v4
	v_or_b32_e32 v8, 0x400, v4
	v_or_b32_e32 v10, 0x600, v4
	s_add_i32 s10, 0, 0x22c38
	v_add_u32_e32 v16, v5, v11
	v_and_b32_e32 v13, 0xfc, v179
	s_mov_b32 s1, 0
	v_mov_b32_e32 v3, 0
	s_mov_b32 s3, 0x100000
	v_mov_b32_e32 v15, s10
	s_movk_i32 s11, 0x833
	s_movk_i32 s12, 0x800
	s_mov_b32 s13, 0x1104e000
	s_movk_i32 s14, 0x7cc
	v_add_u32_e32 v17, 0x404, v16
	v_add_u32_e32 v18, 0x40c, v16
	v_add_u32_e32 v19, 0x808, v16
	v_add_u32_e32 v20, 0xc0c, v16
	v_add_u32_e32 v21, 0xc14, v16
	v_add_u32_e32 v22, 0x1414, v16
	v_add_u32_e32 v23, 0x141c, v16
	v_add_u32_e32 v24, 0x1818, v16
	v_add_u32_e32 v25, 0x1c1c, v16
	v_add_u32_e32 v26, 0x1c24, v16
	v_lshlrev_b32_e32 v2, 1, v2
	v_add_u32_e32 v27, v7, v9
	v_lshlrev_b32_e32 v4, 1, v4
	v_lshlrev_b32_e32 v6, 1, v6
	v_lshlrev_b32_e32 v8, 1, v8
	v_lshlrev_b32_e32 v10, 1, v10
	s_branch .LBB0_2280

; __device__ __forceinline__ unsigned g8_cvt_pk(float lo, float hi) { unsigned r; asm volatile("v_cvt_pk_bf16_f32 %0, %1, %2" : "=v"(r) : "v"(lo), "v"(hi)); return r; }
; __device__ __forceinline__ void convert_deferred(const Ptrs& P, unsigned char* lds, int quota) {
;     ...
;     for (int n = 0; n < quota; ++n) {
;         __syncthreads();
;         if (tid == 0) *slot = (int)atomicAdd(q, 1u);
;         __syncthreads();
;         const int t = *slot;
;         if (t >= DEF_GU + DEF_DN) break;
;         const bool gu = t < DEF_GU;
;         const float* src = gu ? P.in[34] : P.in[36]; bf16* dst = (bf16*)(P.ws + (gu ? WS_WGU : WS_WDN));
;         const int N = gu ? 2048 : 1024, ntn = N / 256, it = gu ? 2 * NE * 16 * 8 - DEF_GU + t : 2 * NE * 16 * 4 - DEF_DN + (t - DEF_GU);
;         f32x4 cur[8];
;         bt_load(src, N, gu ? 1 : 0, it, ntn, cur);
; #pragma unroll
;         for (int i = 0; i < 8; ++i) { float* tp = tile + (wid * 8 + i) * 257 + lane * 4; tp[0] = cur[i][0]; tp[1] = cur[i][1]; tp[2] = cur[i][2]; tp[3] = cur[i][3]; }
;         __syncthreads();
;         const int per = 16 * ntn, z = it / per, r = it % per, kt = r / ntn, nt = r % ntn;
;         bf16* d = dst + (size_t)z * N * 1024 + (((size_t)nt * 16 + kt) << 14);
;         const int kc = lane & 7;
; #pragma unroll
;         for (int pss = 0; pss < 4; ++pss) {
;             const int nn = wid * 32 + pss * 8 + (lane >> 3); float f[8];
; #pragma unroll
;             for (int j = 0; j < 8; ++j) f[j] = tile[(kc * 8 + j) * 257 + nn];
;             u32x4 w; w.x = g8_cvt_pk(f[0], f[1]); w.y = g8_cvt_pk(f[2], f[3]); w.z = g8_cvt_pk(f[4], f[5]); w.w = g8_cvt_pk(f[6], f[7]);
;             *(u32x4*)(d + nn * 64 + kc * 8) = w;
;         }
.LBB0_2284:
	s_or_b64 exec, exec, s[4:5]
	s_waitcnt lgkmcnt(0)
	s_barrier
	ds_read_b32 v5, v15
	s_mov_b64 s[4:5], -1
	s_waitcnt lgkmcnt(0)
	v_cmp_lt_i32_e32 vcc, s11, v5
	v_readfirstlane_b32 s0, v5
	s_cbranch_vccnz .LBB0_2279
	s_cmpk_gt_i32 s0, 0x577
	s_cselect_b64 vcc, -1, 0
	s_and_b64 s[4:5], vcc, exec
	s_cselect_b32 s4, s13, 0x104e000
	s_cselect_b32 s9, 0x400, s12
	s_cselect_b32 s15, s73, s69
	s_cselect_b32 s18, s72, s68
	s_cselect_b32 s5, s14, 0x1a88
	s_cselect_b32 s16, 20, 21
	s_cselect_b32 s19, 10, 11
	s_add_u32 s22, s78, s4
	s_addc_u32 s23, s79, 0
	s_lshr_b32 s6, s9, 4
	s_abs_i32 s4, s6
	v_cvt_f32_u32_e32 v5, s4
	s_sub_i32 s17, 0, s4
	s_add_i32 s5, s5, s0
	s_abs_i32 s7, s5
	v_rcp_iflag_f32_e32 v5, v5
	s_xor_b32 s0, s5, s6
	s_lshr_b32 s8, s9, 8
	s_ashr_i32 s0, s0, 31
	v_mul_f32_e32 v5, 0x4f7ffffe, v5
	v_cvt_u32_f32_e32 v5, v5
	s_nop 0
	v_readfirstlane_b32 s24, v5
	s_mul_i32 s17, s17, s24
	s_mul_hi_u32 s17, s24, s17
	s_add_i32 s24, s24, s17
	s_mul_hi_u32 s17, s7, s24
	s_mul_i32 s24, s17, s4
	s_sub_i32 s7, s7, s24
	s_add_i32 s24, s17, 1
	s_sub_i32 s25, s7, s4
	s_cmp_ge_u32 s7, s4
	s_cselect_b32 s17, s24, s17
	s_cselect_b32 s7, s25, s7
	s_add_i32 s24, s17, 1
	s_cmp_ge_u32 s7, s4
	s_cselect_b32 s4, s24, s17
	s_xor_b32 s4, s4, s0
	s_sub_i32 s4, s4, s0
	s_sext_i32_i8 s0, s8
	v_cvt_f32_i32_e32 v5, s0
	s_mul_i32 s6, s4, s6
	s_sub_i32 s5, s5, s6
	v_cvt_f32_i32_e32 v7, s5
	v_rcp_iflag_f32_e32 v9, v5
	s_xor_b32 s0, s5, s0
	s_ashr_i32 s0, s0, 30
	s_or_b32 s0, s0, 1
	v_mul_f32_e32 v9, v7, v9
	v_trunc_f32_e32 v9, v9
	v_fma_f32 v7, -v9, v5, v7
	v_cvt_i32_f32_e32 v9, v9
	v_cmp_ge_f32_e64 s[6:7], |v7|, |v5|
	s_and_b64 s[6:7], s[6:7], exec
	s_cselect_b32 s0, s0, 0
	v_readfirstlane_b32 s6, v9
	s_add_i32 s6, s6, s0
	s_mul_i32 s7, s6, s8
	s_sub_i32 s8, s5, s7
	s_sext_i32_i8 s5, s8
	v_lshl_add_u32 v5, s5, 7, v12
	v_lshl_or_b32 v7, s5, 8, v13
	s_ashr_i32 s5, s4, 31
	s_sext_i32_i8 s0, s6
	s_lshl_b64 s[16:17], s[4:5], s16
	v_lshl_or_b32 v30, s0, 6, v14
	s_lshl_b64 s[16:17], s[16:17], 2
	v_ashrrev_i32_e32 v31, 31, v30
	s_add_u32 s16, s18, s16
	v_cndmask_b32_e32 v28, v5, v7, vcc
	s_addc_u32 s17, s15, s17
	v_lshlrev_b64 v[30:31], s19, v[30:31]
	v_lshl_add_u64 v[30:31], v[30:31], 2, s[16:17]
	v_ashrrev_i32_e32 v29, 31, v28
	v_lshl_add_u64 v[52:53], v[28:29], 2, v[30:31]
	s_lshl_b32 s0, s9, 2
	s_lshl_b64 s[16:17], 12, s19
	v_lshl_add_u64 v[36:37], v[52:53], 0, s[0:1]
	v_lshl_add_u64 v[44:45], v[52:53], 0, s[16:17]
	s_lshl_b64 s[16:17], 24, s19
	v_lshl_add_u64 v[54:55], v[36:37], 0, s[0:1]
	v_lshl_add_u64 v[56:57], v[52:53], 0, s[16:17]
	s_lshl_b64 s[16:17], 28, s19
	s_lshl_b32 s0, s9, 3
	v_lshl_add_u64 v[58:59], v[52:53], 0, s[16:17]
	v_lshl_add_u64 v[60:61], v[54:55], 0, s[0:1]
	s_lshl_b64 s[16:17], 20, s19
	global_load_dwordx4 v[28:31], v[52:53], off nt
	global_load_dwordx4 v[32:35], v[36:37], off nt
	s_nop 0
	global_load_dwordx4 v[36:39], v[54:55], off nt
	global_load_dwordx4 v[40:43], v[44:45], off nt
	s_nop 0
	global_load_dwordx4 v[44:47], v[56:57], off nt
	global_load_dwordx4 v[48:51], v[58:59], off nt
	v_lshl_add_u64 v[62:63], v[52:53], 0, s[16:17]
	global_load_dwordx4 v[52:55], v[60:61], off nt
	global_load_dwordx4 v[56:59], v[62:63], off nt
	s_lshl_b64 s[4:5], s[4:5], s19
	s_lshl_b64 s[4:5], s[4:5], 11
	s_add_u32 s0, s22, s4
	s_addc_u32 s9, s23, s5
	s_bfe_i64 s[4:5], s[8:9], 0x80000
	s_bfe_i64 s[6:7], s[6:7], 0x80000
	s_lshl_b64 s[4:5], s[4:5], 19
	s_add_u32 s0, s0, s4
	s_addc_u32 s8, s9, s5
	s_lshl_b64 s[4:5], s[6:7], 15
	s_add_u32 s4, s0, s4
	s_addc_u32 s5, s8, s5
	v_mov_b32_e32 v5, v3
	s_add_i32 s3, s3, -1
	s_cmp_eq_u32 s3, 0
	s_waitcnt vmcnt(7)
	ds_write_b128 v16, v[28:31]
	s_waitcnt vmcnt(6)
	ds_write2_b32 v17, v32, v33 offset1:1
	ds_write2_b32 v18, v34, v35 offset1:1
	s_waitcnt vmcnt(3)
	ds_write2_b64 v24, v[44:45], v[46:47] offset1:1
	s_waitcnt vmcnt(2)
	ds_write2_b32 v25, v48, v49 offset1:1
	ds_write2_b32 v26, v50, v51 offset1:1
	ds_write2_b64 v19, v[36:37], v[38:39] offset1:1
	ds_write2_b32 v20, v40, v41 offset1:1
	ds_write2_b32 v21, v42, v43 offset1:1
	s_waitcnt vmcnt(1)
	ds_write_b128 v16, v[52:55] offset:4112
	s_waitcnt vmcnt(0)
	ds_write2_b32 v22, v56, v57 offset1:1
	ds_write2_b32 v23, v58, v59 offset1:1
	s_waitcnt lgkmcnt(0)
	s_barrier
	ds_read_b32 v7, v27 offset:1028
	ds_read_b32 v9, v27 offset:3084
	ds_read_b32 v11, v27 offset:5140
	ds_read_b32 v31, v27 offset:7196
	ds_read_b32 v32, v27 offset:6168
	ds_read_b32 v30, v27 offset:4112
	ds_read_b32 v29, v27 offset:2056
	ds_read_b32 v28, v27
	s_waitcnt lgkmcnt(0)
	v_cvt_pk_bf16_f32 v28, v28, v7
	v_cvt_pk_bf16_f32 v29, v29, v9
	v_cvt_pk_bf16_f32 v30, v30, v11
	v_cvt_pk_bf16_f32 v31, v32, v31
	ds_read_b32 v7, v27 offset:1060
	ds_read_b32 v9, v27 offset:3116
	ds_read_b32 v11, v27 offset:5172
	ds_read_b32 v36, v27 offset:7228
	ds_read_b32 v37, v27 offset:6200
	ds_read_b32 v38, v27 offset:4144
	ds_read_b32 v39, v27 offset:2088
	ds_read_b32 v40, v27 offset:32
	v_lshl_add_u64 v[32:33], s[4:5], 0, v[2:3]
	v_lshl_add_u64 v[34:35], v[32:33], 0, v[4:5]
	global_store_dwordx4 v[34:35], v[28:31], off
	s_cselect_b64 s[4:5], -1, 0
	s_waitcnt lgkmcnt(0)
	v_cvt_pk_bf16_f32 v28, v40, v7
	v_cvt_pk_bf16_f32 v29, v39, v9
	v_cvt_pk_bf16_f32 v30, v38, v11
	v_cvt_pk_bf16_f32 v31, v37, v36
	ds_read_b32 v5, v27 offset:1092
	ds_read_b32 v9, v27 offset:3148
	ds_read_b32 v11, v27 offset:5204
	ds_read_b32 v36, v27 offset:6232
	ds_read_b32 v37, v27 offset:4176
	ds_read_b32 v38, v27 offset:2120
	ds_read_b32 v39, v27 offset:64
	ds_read_b32 v40, v27 offset:7260
	v_mov_b32_e32 v7, v3
	v_lshl_add_u64 v[34:35], v[32:33], 0, v[6:7]
	global_store_dwordx4 v[34:35], v[28:31], off
	s_waitcnt lgkmcnt(1)
	s_nop 0
	v_cvt_pk_bf16_f32 v28, v39, v5
	v_cvt_pk_bf16_f32 v29, v38, v9
	v_cvt_pk_bf16_f32 v30, v37, v11
	s_waitcnt lgkmcnt(0)
	v_cvt_pk_bf16_f32 v31, v36, v40
	ds_read_b32 v5, v27 offset:1124
	ds_read_b32 v7, v27 offset:3180
	ds_read_b32 v11, v27 offset:5236
	ds_read_b32 v36, v27 offset:6264
	ds_read_b32 v37, v27 offset:4208
	ds_read_b32 v38, v27 offset:2152
	ds_read_b32 v39, v27 offset:96
	ds_read_b32 v40, v27 offset:7292
	v_mov_b32_e32 v9, v3
	v_lshl_add_u64 v[34:35], v[32:33], 0, v[8:9]
	global_store_dwordx4 v[34:35], v[28:31], off
	s_waitcnt lgkmcnt(1)
	s_nop 0
	v_cvt_pk_bf16_f32 v28, v39, v5
	v_cvt_pk_bf16_f32 v29, v38, v7
	v_cvt_pk_bf16_f32 v30, v37, v11
	v_mov_b32_e32 v11, v3
	v_lshl_add_u64 v[32:33], v[32:33], 0, v[10:11]
	s_waitcnt lgkmcnt(0)
	v_cvt_pk_bf16_f32 v31, v36, v40
	global_store_dwordx4 v[32:33], v[28:31], off
	s_branch .LBB0_2279
